# packed f32 VALU ops beside MFMAs split into scalar pairs (scan decay multiplies; fox/dsa/ret attention tile loops)
# speedup vs baseline: 1.0062x; 1.0031x over previous
.LBB0_490:
	s_bitcmp1_b32 s35, 0
	s_cselect_b32 s26, 0xea00, 0
	v_add_u32_e32 v159, s26, v157
	v_add_u32_e32 v190, v159, v155
	ds_read2_b64 v[68:71], v190 offset1:2
	ds_read2_b64 v[84:87], v190 offset0:4 offset1:6
	ds_read2_b64 v[88:91], v190 offset0:8 offset1:10
	ds_read2_b64 v[92:95], v190 offset0:12 offset1:14
	ds_read2_b64 v[96:99], v190 offset0:16 offset1:18
	ds_read2_b64 v[100:103], v190 offset0:20 offset1:22
	ds_read2_b64 v[104:107], v190 offset0:24 offset1:26
	ds_read2_b64 v[108:111], v190 offset0:28 offset1:30
	v_cvt_pk_bf16_f32 v116, v52, v53
	v_cvt_pk_bf16_f32 v117, v54, v55
	v_cvt_pk_bf16_f32 v118, v56, v57
	v_cvt_pk_bf16_f32 v119, v58, v59
	v_cvt_pk_bf16_f32 v120, v60, v61
	v_cvt_pk_bf16_f32 v121, v62, v63
	v_cvt_pk_bf16_f32 v122, v64, v65
	v_cvt_pk_bf16_f32 v123, v66, v67
	v_cvt_pk_bf16_f32 v124, v36, v37
	v_cvt_pk_bf16_f32 v125, v38, v39
	v_cvt_pk_bf16_f32 v126, v40, v41
	v_cvt_pk_bf16_f32 v127, v42, v43
	v_cvt_pk_bf16_f32 v128, v44, v45
	v_cvt_pk_bf16_f32 v129, v46, v47
	v_cvt_pk_bf16_f32 v130, v48, v49
	v_cvt_pk_bf16_f32 v131, v50, v51
	v_cvt_pk_bf16_f32 v132, v20, v21
	v_cvt_pk_bf16_f32 v133, v22, v23
	v_cvt_pk_bf16_f32 v134, v24, v25
	v_cvt_pk_bf16_f32 v135, v26, v27
	v_cvt_pk_bf16_f32 v136, v28, v29
	v_cvt_pk_bf16_f32 v137, v30, v31
	v_cvt_pk_bf16_f32 v138, v32, v33
	v_cvt_pk_bf16_f32 v139, v34, v35
	v_cvt_pk_bf16_f32 v140, v4, v5
	v_cvt_pk_bf16_f32 v141, v6, v7
	v_cvt_pk_bf16_f32 v142, v8, v9
	v_cvt_pk_bf16_f32 v143, v10, v11
	v_cvt_pk_bf16_f32 v144, v12, v13
	v_cvt_pk_bf16_f32 v145, v14, v15
	v_cvt_pk_bf16_f32 v146, v16, v17
	v_cvt_pk_bf16_f32 v147, v18, v19
	s_waitcnt lgkmcnt(0)
	v_mfma_f32_32x32x16_bf16 v[68:83], v[68:71], v[116:119], 0
	v_mfma_f32_32x32x16_bf16 v[68:83], v[84:87], v[120:123], v[68:83]
	v_mfma_f32_32x32x16_bf16 v[68:83], v[88:91], v[124:127], v[68:83]
	v_mfma_f32_32x32x16_bf16 v[68:83], v[92:95], v[128:131], v[68:83]
	v_mfma_f32_32x32x16_bf16 v[68:83], v[96:99], v[132:135], v[68:83]
	v_mfma_f32_32x32x16_bf16 v[68:83], v[100:103], v[136:139], v[68:83]
	v_mfma_f32_32x32x16_bf16 v[68:83], v[104:107], v[140:143], v[68:83]
	v_mfma_f32_32x32x16_bf16 v[68:83], v[108:111], v[144:147], v[68:83]
	v_add_u32_e32 v88, 0x2000, v190
	ds_read2_b64 v[84:87], v88 offset0:32 offset1:34
	ds_read2_b64 v[100:103], v88 offset0:36 offset1:38
	ds_read2_b64 v[104:107], v88 offset0:40 offset1:42
	ds_read2_b64 v[108:111], v88 offset0:44 offset1:46
	ds_read2_b64 v[112:115], v88 offset0:48 offset1:50
	ds_read2_b64 v[182:185], v88 offset0:52 offset1:54
	ds_read2_b64 v[186:189], v88 offset0:56 offset1:58
	ds_read2_b64 v[214:217], v88 offset0:60 offset1:62
	s_waitcnt lgkmcnt(0)
	v_mfma_f32_32x32x16_bf16 v[84:99], v[84:87], v[116:119], 0
	v_mfma_f32_32x32x16_bf16 v[84:99], v[100:103], v[120:123], v[84:99]
	v_mfma_f32_32x32x16_bf16 v[84:99], v[104:107], v[124:127], v[84:99]
	v_mfma_f32_32x32x16_bf16 v[84:99], v[108:111], v[128:131], v[84:99]
	v_mfma_f32_32x32x16_bf16 v[84:99], v[112:115], v[132:135], v[84:99]
	v_mfma_f32_32x32x16_bf16 v[84:99], v[182:185], v[136:139], v[84:99]
	v_mfma_f32_32x32x16_bf16 v[84:99], v[186:189], v[140:143], v[84:99]
	v_mfma_f32_32x32x16_bf16 v[84:99], v[214:217], v[144:147], v[84:99]
	s_waitcnt vmcnt(32)
	v_mov_b32_e32 v200, v201
	v_sub_f32_e32 v81, v197, v81
	v_sub_f32_e32 v80, v196, v80
	v_sub_f32_e32 v71, v165, v71
	v_sub_f32_e32 v70, v164, v70
	v_sub_f32_e32 v69, v167, v69
	v_sub_f32_e32 v68, v166, v68
	v_cvt_pk_bf16_f32 v106, v80, v81
	s_nop 3
	v_sub_f32_e32 v80, v175, v87
	v_sub_f32_e32 v81, v174, v86
	v_sub_f32_e32 v83, v199, v83
	v_sub_f32_e32 v82, v198, v82
	v_sub_f32_e32 v79, v195, v79
	v_sub_f32_e32 v78, v194, v78
	v_sub_f32_e32 v77, v181, v77
	v_sub_f32_e32 v76, v180, v76
	v_sub_f32_e32 v75, v171, v75
	v_sub_f32_e32 v74, v170, v74
	v_sub_f32_e32 v73, v169, v73
	v_sub_f32_e32 v72, v168, v72
	v_cvt_pk_bf16_f32 v100, v68, v69
	v_cvt_pk_bf16_f32 v101, v70, v71
	v_sub_f32_e32 v68, v179, v91
	v_sub_f32_e32 v69, v178, v90
	v_sub_f32_e32 v70, v177, v89
	v_sub_f32_e32 v71, v176, v88
	v_cvt_pk_bf16_f32 v109, v81, v80
	v_add_u32_e32 v80, 0x4000, v190
	v_cvt_pk_bf16_f32 v102, v72, v73
	v_cvt_pk_bf16_f32 v103, v74, v75
	v_cvt_pk_bf16_f32 v104, v76, v77
	v_cvt_pk_bf16_f32 v105, v78, v79
	v_cvt_pk_bf16_f32 v107, v82, v83
	v_sub_f32_e32 v72, v209, v99
	v_sub_f32_e32 v73, v208, v98
	v_sub_f32_e32 v74, v207, v97
	v_sub_f32_e32 v75, v206, v96
	v_sub_f32_e32 v76, v205, v95
	v_sub_f32_e32 v77, v204, v94
	v_sub_f32_e32 v78, v203, v93
	v_sub_f32_e32 v79, v202, v92
	v_sub_f32_e32 v82, v173, v85
	v_sub_f32_e32 v83, v172, v84
	v_cvt_pk_bf16_f32 v110, v71, v70
	v_cvt_pk_bf16_f32 v111, v69, v68
	ds_read2_b64 v[68:71], v80 offset0:64 offset1:66
	ds_read2_b64 v[84:87], v80 offset0:68 offset1:70
	ds_read2_b64 v[88:91], v80 offset0:72 offset1:74
	ds_read2_b64 v[92:95], v80 offset0:76 offset1:78
	ds_read2_b64 v[96:99], v80 offset0:80 offset1:82
	ds_read2_b64 v[164:167], v80 offset0:84 offset1:86
	ds_read2_b64 v[168:171], v80 offset0:88 offset1:90
	ds_read2_b64 v[172:175], v80 offset0:92 offset1:94
	v_cvt_pk_bf16_f32 v108, v83, v82
	v_cvt_pk_bf16_f32 v112, v79, v78
	v_cvt_pk_bf16_f32 v113, v77, v76
	v_cvt_pk_bf16_f32 v114, v75, v74
	v_cvt_pk_bf16_f32 v115, v73, v72
	s_waitcnt lgkmcnt(7)
	v_mfma_f32_32x32x16_bf16 v[68:83], v[68:71], v[116:119], 0
	s_waitcnt lgkmcnt(6)
	v_mfma_f32_32x32x16_bf16 v[68:83], v[84:87], v[120:123], v[68:83]
	s_waitcnt lgkmcnt(5)
	v_mfma_f32_32x32x16_bf16 v[68:83], v[88:91], v[124:127], v[68:83]
	s_waitcnt lgkmcnt(4)
	v_mfma_f32_32x32x16_bf16 v[68:83], v[92:95], v[128:131], v[68:83]
	s_waitcnt lgkmcnt(3)
	v_mfma_f32_32x32x16_bf16 v[68:83], v[96:99], v[132:135], v[68:83]
	s_waitcnt lgkmcnt(2)
	v_mfma_f32_32x32x16_bf16 v[68:83], v[164:167], v[136:139], v[68:83]
	s_waitcnt lgkmcnt(1)
	v_mfma_f32_32x32x16_bf16 v[68:83], v[168:171], v[140:143], v[68:83]
	s_waitcnt lgkmcnt(0)
	v_mfma_f32_32x32x16_bf16 v[68:83], v[172:175], v[144:147], v[68:83]
	v_add_u32_e32 v88, 0x6000, v190
	ds_read2_b64 v[84:87], v88 offset0:96 offset1:98
	ds_read2_b64 v[164:167], v88 offset0:100 offset1:102
	ds_read2_b64 v[168:171], v88 offset0:104 offset1:106
	ds_read2_b64 v[172:175], v88 offset0:108 offset1:110
	ds_read2_b64 v[176:179], v88 offset0:112 offset1:114
	ds_read2_b64 v[180:183], v88 offset0:116 offset1:118
	ds_read2_b64 v[184:187], v88 offset0:120 offset1:122
	ds_read2_b64 v[194:197], v88 offset0:124 offset1:126
	s_waitcnt lgkmcnt(7)
	v_mfma_f32_32x32x16_bf16 v[84:99], v[84:87], v[116:119], 0
	s_waitcnt lgkmcnt(6)
	v_mfma_f32_32x32x16_bf16 v[84:99], v[164:167], v[120:123], v[84:99]
	s_waitcnt lgkmcnt(5)
	v_mfma_f32_32x32x16_bf16 v[84:99], v[168:171], v[124:127], v[84:99]
	s_waitcnt lgkmcnt(4)
	v_mfma_f32_32x32x16_bf16 v[84:99], v[172:175], v[128:131], v[84:99]
	s_waitcnt lgkmcnt(3)
	v_mfma_f32_32x32x16_bf16 v[84:99], v[176:179], v[132:135], v[84:99]
	s_waitcnt lgkmcnt(2)
	v_mfma_f32_32x32x16_bf16 v[84:99], v[180:183], v[136:139], v[84:99]
	s_waitcnt lgkmcnt(1)
	v_mfma_f32_32x32x16_bf16 v[84:99], v[184:187], v[140:143], v[84:99]
	s_waitcnt lgkmcnt(0)
	v_mfma_f32_32x32x16_bf16 v[84:99], v[194:197], v[144:147], v[84:99]
	v_add_u32_e32 v159, v159, v153
	v_add_u32_e32 v128, 0x8000, v159
	v_add_u32_e32 v144, 0x9000, v159
	ds_read2_b64 v[116:119], v128 offset0:128 offset1:130
	ds_read2_b64 v[120:123], v128 offset0:132 offset1:134
	ds_read2_b64 v[124:127], v128 offset0:136 offset1:138
	ds_read2_b64 v[128:131], v128 offset0:140 offset1:142
	ds_read2_b64 v[132:135], v144 offset0:160 offset1:162
	ds_read2_b64 v[136:139], v144 offset0:164 offset1:166
	ds_read2_b64 v[140:143], v144 offset0:168 offset1:170
	ds_read2_b64 v[144:147], v144 offset0:172 offset1:174
	s_waitcnt lgkmcnt(7)
	v_mfma_f32_32x32x16_bf16 v[68:83], v[116:119], v[100:103], v[68:83]
	s_waitcnt lgkmcnt(3)
	v_mfma_f32_32x32x16_bf16 v[84:99], v[132:135], v[100:103], v[84:99]
	v_mfma_f32_32x32x16_bf16 v[68:83], v[120:123], v[104:107], v[68:83]
	s_waitcnt lgkmcnt(2)
	v_mfma_f32_32x32x16_bf16 v[84:99], v[136:139], v[104:107], v[84:99]
	v_mfma_f32_32x32x16_bf16 v[68:83], v[124:127], v[108:111], v[68:83]
	s_waitcnt lgkmcnt(1)
	v_mfma_f32_32x32x16_bf16 v[84:99], v[140:143], v[108:111], v[84:99]
	v_mfma_f32_32x32x16_bf16 v[68:83], v[128:131], v[112:115], v[68:83]
	s_waitcnt lgkmcnt(0)
	v_mfma_f32_32x32x16_bf16 v[84:99], v[144:147], v[112:115], v[84:99]
	v_lshl_add_u64 v[116:117], s[6:7], 0, v[162:163]
	s_mov_b32 s26, 0x41a20000
	v_add_co_u32_e32 v218, vcc, s26, v116
	s_nop 1
	v_addc_co_u32_e32 v219, vcc, 0, v117, vcc
	s_mov_b32 s26, 0x41a21000
	v_add_co_u32_e32 v220, vcc, s26, v116
	s_nop 1
	v_addc_co_u32_e32 v221, vcc, 0, v117, vcc
	s_mov_b32 s26, 0x41a24000
	v_add_co_u32_e32 v222, vcc, s26, v116
	s_nop 1
	v_addc_co_u32_e32 v223, vcc, 0, v117, vcc
	s_mov_b32 s26, 0x41a25000
	v_add_co_u32_e32 v224, vcc, s26, v116
	s_nop 1
	v_addc_co_u32_e32 v225, vcc, 0, v117, vcc
	global_load_dword v166, v[218:219], off
	global_load_dword v167, v[218:219], off offset:2048
	global_load_dword v164, v[220:221], off
	global_load_dword v165, v[220:221], off offset:2048
	global_load_dword v168, v[222:223], off
	global_load_dword v169, v[222:223], off offset:2048
	global_load_dword v170, v[224:225], off
	global_load_dword v171, v[224:225], off offset:2048
	s_mov_b32 s26, 0x41a28000
	v_add_co_u32_e32 v218, vcc, s26, v116
	s_nop 1
	v_addc_co_u32_e32 v219, vcc, 0, v117, vcc
	s_mov_b32 s26, 0x41a29000
	v_add_co_u32_e32 v220, vcc, s26, v116
	s_nop 1
	v_addc_co_u32_e32 v221, vcc, 0, v117, vcc
	s_mov_b32 s26, 0x41a2c000
	v_add_co_u32_e32 v222, vcc, s26, v116
	s_nop 1
	v_addc_co_u32_e32 v223, vcc, 0, v117, vcc
	s_mov_b32 s26, 0x41a2d000
	v_add_co_u32_e32 v224, vcc, s26, v116
	s_nop 1
	v_addc_co_u32_e32 v225, vcc, 0, v117, vcc
	global_load_dword v180, v[218:219], off
	global_load_dword v181, v[218:219], off offset:2048
	global_load_dword v194, v[220:221], off
	global_load_dword v195, v[220:221], off offset:2048
	global_load_dword v196, v[222:223], off
	global_load_dword v197, v[222:223], off offset:2048
	global_load_dword v198, v[224:225], off
	global_load_dword v199, v[224:225], off offset:2048
	s_mov_b32 s26, 0x41a30000
	v_add_co_u32_e32 v218, vcc, s26, v116
	s_nop 1
	v_addc_co_u32_e32 v219, vcc, 0, v117, vcc
	s_mov_b32 s26, 0x41a31000
	v_add_co_u32_e32 v220, vcc, s26, v116
	s_nop 1
	v_addc_co_u32_e32 v221, vcc, 0, v117, vcc
	s_mov_b32 s26, 0x41a34000
	v_add_co_u32_e32 v222, vcc, s26, v116
	s_nop 1
	v_addc_co_u32_e32 v223, vcc, 0, v117, vcc
	s_mov_b32 s26, 0x41a35000
	v_add_co_u32_e32 v224, vcc, s26, v116
	s_nop 1
	v_addc_co_u32_e32 v225, vcc, 0, v117, vcc
	global_load_dword v172, v[218:219], off
	global_load_dword v173, v[218:219], off offset:2048
	global_load_dword v174, v[220:221], off
	global_load_dword v175, v[220:221], off offset:2048
	global_load_dword v176, v[222:223], off
	global_load_dword v177, v[222:223], off offset:2048
	global_load_dword v178, v[224:225], off
	global_load_dword v179, v[224:225], off offset:2048
	s_mov_b32 s26, 0x41a38000
	v_add_co_u32_e32 v218, vcc, s26, v116
	s_nop 1
	v_addc_co_u32_e32 v219, vcc, 0, v117, vcc
	s_mov_b32 s26, 0x41a39000
	v_add_co_u32_e32 v220, vcc, s26, v116
	s_nop 1
	v_addc_co_u32_e32 v221, vcc, 0, v117, vcc
	s_mov_b32 s26, 0x41a3c000
	v_add_co_u32_e32 v222, vcc, s26, v116
	s_nop 1
	v_addc_co_u32_e32 v223, vcc, 0, v117, vcc
	s_mov_b32 s26, 0x41a3d000
	v_add_co_u32_e32 v224, vcc, s26, v116
	s_nop 1
	v_addc_co_u32_e32 v225, vcc, 0, v117, vcc
	global_load_dword v202, v[218:219], off
	global_load_dword v203, v[218:219], off offset:2048
	global_load_dword v204, v[220:221], off
	global_load_dword v205, v[220:221], off offset:2048
	global_load_dword v206, v[222:223], off
	global_load_dword v207, v[222:223], off offset:2048
	global_load_dword v208, v[224:225], off
	global_load_dword v209, v[224:225], off offset:2048
	s_add_i32 s35, s35, 1
	s_add_u32 s26, s6, s28
	s_addc_u32 s27, s7, s29
	v_mov_b64_e32 v[232:233], s[26:27]
	global_load_dword v201, v[232:233], off
	s_mov_b32 s26, 0x47200000
	v_add_co_u32_e32 v218, vcc, s26, v116
	s_nop 1
	v_addc_co_u32_e32 v219, vcc, 0, v117, vcc
	s_mov_b32 s26, 0x47201000
	v_add_co_u32_e32 v220, vcc, s26, v116
	s_nop 1
	v_addc_co_u32_e32 v221, vcc, 0, v117, vcc
	s_mov_b32 s26, 0x47204000
	v_add_co_u32_e32 v222, vcc, s26, v116
	s_nop 1
	v_addc_co_u32_e32 v223, vcc, 0, v117, vcc
	s_mov_b32 s26, 0x47205000
	v_add_co_u32_e32 v224, vcc, s26, v116
	s_nop 1
	v_addc_co_u32_e32 v225, vcc, 0, v117, vcc
	global_store_dword v[218:219], v68, off
	global_store_dword v[218:219], v69, off offset:2048
	global_store_dword v[220:221], v70, off
	global_store_dword v[220:221], v71, off offset:2048
	global_store_dword v[222:223], v72, off
	global_store_dword v[222:223], v73, off offset:2048
	global_store_dword v[224:225], v74, off
	global_store_dword v[224:225], v75, off offset:2048
	s_mov_b32 s26, 0x47208000
	v_add_co_u32_e32 v218, vcc, s26, v116
	s_nop 1
	v_addc_co_u32_e32 v219, vcc, 0, v117, vcc
	s_mov_b32 s26, 0x47209000
	v_add_co_u32_e32 v220, vcc, s26, v116
	s_nop 1
	v_addc_co_u32_e32 v221, vcc, 0, v117, vcc
	s_mov_b32 s26, 0x4720c000
	v_add_co_u32_e32 v222, vcc, s26, v116
	s_nop 1
	v_addc_co_u32_e32 v223, vcc, 0, v117, vcc
	s_mov_b32 s26, 0x4720d000
	v_add_co_u32_e32 v224, vcc, s26, v116
	s_nop 1
	v_addc_co_u32_e32 v225, vcc, 0, v117, vcc
	global_store_dword v[218:219], v76, off
	global_store_dword v[218:219], v77, off offset:2048
	global_store_dword v[220:221], v78, off
	global_store_dword v[220:221], v79, off offset:2048
	global_store_dword v[222:223], v80, off
	global_store_dword v[222:223], v81, off offset:2048
	global_store_dword v[224:225], v82, off
	global_store_dword v[224:225], v83, off offset:2048
	s_mov_b32 s26, 0x47210000
	v_add_co_u32_e32 v218, vcc, s26, v116
	s_nop 1
	v_addc_co_u32_e32 v219, vcc, 0, v117, vcc
	s_mov_b32 s26, 0x47211000
	v_add_co_u32_e32 v220, vcc, s26, v116
	s_nop 1
	v_addc_co_u32_e32 v221, vcc, 0, v117, vcc
	s_mov_b32 s26, 0x47214000
	v_add_co_u32_e32 v222, vcc, s26, v116
	s_nop 1
	v_addc_co_u32_e32 v223, vcc, 0, v117, vcc
	s_mov_b32 s26, 0x47215000
	v_add_co_u32_e32 v224, vcc, s26, v116
	s_nop 1
	v_addc_co_u32_e32 v225, vcc, 0, v117, vcc
	global_store_dword v[218:219], v84, off
	global_store_dword v[218:219], v85, off offset:2048
	global_store_dword v[220:221], v86, off
	global_store_dword v[220:221], v87, off offset:2048
	global_store_dword v[222:223], v88, off
	global_store_dword v[222:223], v89, off offset:2048
	global_store_dword v[224:225], v90, off
	global_store_dword v[224:225], v91, off offset:2048
	s_mov_b32 s26, 0x47218000
	v_add_co_u32_e32 v218, vcc, s26, v116
	s_nop 1
	v_addc_co_u32_e32 v219, vcc, 0, v117, vcc
	s_mov_b32 s26, 0x47219000
	v_add_co_u32_e32 v220, vcc, s26, v116
	s_nop 1
	v_addc_co_u32_e32 v221, vcc, 0, v117, vcc
	s_mov_b32 s26, 0x4721c000
	v_add_co_u32_e32 v222, vcc, s26, v116
	s_nop 1
	v_addc_co_u32_e32 v223, vcc, 0, v117, vcc
	s_mov_b32 s26, 0x4721d000
	v_add_co_u32_e32 v224, vcc, s26, v116
	s_nop 1
	v_addc_co_u32_e32 v225, vcc, 0, v117, vcc
	global_store_dword v[218:219], v92, off
	global_store_dword v[218:219], v93, off offset:2048
	global_store_dword v[220:221], v94, off
	global_store_dword v[220:221], v95, off offset:2048
	global_store_dword v[222:223], v96, off
	global_store_dword v[222:223], v97, off offset:2048
	global_store_dword v[224:225], v98, off
	global_store_dword v[224:225], v99, off offset:2048
	v_add_u32_e32 v80, 0xa000, v159
	v_add_u32_e32 v96, 0xb000, v159
	ds_read2_b64 v[68:71], v80 offset0:192 offset1:194
	ds_read2_b64 v[72:75], v80 offset0:196 offset1:198
	ds_read2_b64 v[76:79], v80 offset0:200 offset1:202
	ds_read2_b64 v[80:83], v80 offset0:204 offset1:206
	ds_read2_b64 v[84:87], v96 offset0:224 offset1:226
	ds_read2_b64 v[88:91], v96 offset0:228 offset1:230
	ds_read2_b64 v[92:95], v96 offset0:232 offset1:234
	ds_read2_b64 v[96:99], v96 offset0:236 offset1:238
	v_mul_f32_e32 v66, v200, v66
	v_mul_f32_e32 v67, v200, v67
	v_mul_f32_e32 v64, v200, v64
	v_mul_f32_e32 v65, v200, v65
	v_mul_f32_e32 v62, v200, v62
	v_mul_f32_e32 v63, v200, v63
	v_mul_f32_e32 v60, v200, v60
	v_mul_f32_e32 v61, v200, v61
	v_mul_f32_e32 v58, v200, v58
	v_mul_f32_e32 v59, v200, v59
	v_mul_f32_e32 v56, v200, v56
	v_mul_f32_e32 v57, v200, v57
	v_mul_f32_e32 v54, v200, v54
	v_mul_f32_e32 v55, v200, v55
	v_mul_f32_e32 v52, v200, v52
	v_mul_f32_e32 v53, v200, v53
	v_mul_f32_e32 v50, v200, v50
	v_mul_f32_e32 v51, v200, v51
	v_mul_f32_e32 v48, v200, v48
	v_mul_f32_e32 v49, v200, v49
	v_mul_f32_e32 v46, v200, v46
	v_mul_f32_e32 v47, v200, v47
	v_mul_f32_e32 v44, v200, v44
	v_mul_f32_e32 v45, v200, v45
	v_mul_f32_e32 v42, v200, v42
	v_mul_f32_e32 v43, v200, v43
	v_mul_f32_e32 v40, v200, v40
	v_mul_f32_e32 v41, v200, v41
	v_mul_f32_e32 v38, v200, v38
	v_mul_f32_e32 v39, v200, v39
	v_mul_f32_e32 v36, v200, v36
	v_mul_f32_e32 v37, v200, v37
	s_waitcnt lgkmcnt(0)
	v_mfma_f32_32x32x16_bf16 v[52:67], v[68:71], v[100:103], v[52:67]
	v_mfma_f32_32x32x16_bf16 v[36:51], v[84:87], v[100:103], v[36:51]
	v_mfma_f32_32x32x16_bf16 v[52:67], v[72:75], v[104:107], v[52:67]
	v_mfma_f32_32x32x16_bf16 v[36:51], v[88:91], v[104:107], v[36:51]
	v_mfma_f32_32x32x16_bf16 v[52:67], v[76:79], v[108:111], v[52:67]
	v_mfma_f32_32x32x16_bf16 v[36:51], v[92:95], v[108:111], v[36:51]
	v_mfma_f32_32x32x16_bf16 v[52:67], v[80:83], v[112:115], v[52:67]
	v_mfma_f32_32x32x16_bf16 v[36:51], v[96:99], v[112:115], v[36:51]
	v_add_u32_e32 v80, 0xc800, v159
	v_add_u32_e32 v96, 0xd800, v159
	ds_read2_b64 v[68:71], v80 offset1:2
	ds_read2_b64 v[72:75], v80 offset0:4 offset1:6
	ds_read2_b64 v[76:79], v80 offset0:8 offset1:10
	ds_read2_b64 v[80:83], v80 offset0:12 offset1:14
	ds_read2_b64 v[84:87], v96 offset0:32 offset1:34
	ds_read2_b64 v[88:91], v96 offset0:36 offset1:38
	ds_read2_b64 v[92:95], v96 offset0:40 offset1:42
	ds_read2_b64 v[96:99], v96 offset0:44 offset1:46
	v_mul_f32_e32 v34, v200, v34
	v_mul_f32_e32 v35, v200, v35
	v_mul_f32_e32 v32, v200, v32
	v_mul_f32_e32 v33, v200, v33
	v_mul_f32_e32 v30, v200, v30
	v_mul_f32_e32 v31, v200, v31
	v_mul_f32_e32 v28, v200, v28
	v_mul_f32_e32 v29, v200, v29
	v_mul_f32_e32 v26, v200, v26
	v_mul_f32_e32 v27, v200, v27
	v_mul_f32_e32 v24, v200, v24
	v_mul_f32_e32 v25, v200, v25
	v_mul_f32_e32 v22, v200, v22
	v_mul_f32_e32 v23, v200, v23
	v_mul_f32_e32 v20, v200, v20
	v_mul_f32_e32 v21, v200, v21
	v_mul_f32_e32 v18, v200, v18
	v_mul_f32_e32 v19, v200, v19
	v_mul_f32_e32 v16, v200, v16
	v_mul_f32_e32 v17, v200, v17
	v_mul_f32_e32 v14, v200, v14
	v_mul_f32_e32 v15, v200, v15
	v_mul_f32_e32 v12, v200, v12
	v_mul_f32_e32 v13, v200, v13
	v_mul_f32_e32 v10, v200, v10
	v_mul_f32_e32 v11, v200, v11
	v_mul_f32_e32 v8, v200, v8
	v_mul_f32_e32 v9, v200, v9
	v_mul_f32_e32 v6, v200, v6
	v_mul_f32_e32 v7, v200, v7
	v_mul_f32_e32 v4, v200, v4
	v_mul_f32_e32 v5, v200, v5
	s_waitcnt lgkmcnt(0)
	v_mfma_f32_32x32x16_bf16 v[20:35], v[68:71], v[100:103], v[20:35]
	v_mfma_f32_32x32x16_bf16 v[4:19], v[84:87], v[100:103], v[4:19]
	v_mfma_f32_32x32x16_bf16 v[20:35], v[72:75], v[104:107], v[20:35]
	v_mfma_f32_32x32x16_bf16 v[4:19], v[88:91], v[104:107], v[4:19]
	v_mfma_f32_32x32x16_bf16 v[20:35], v[76:79], v[108:111], v[20:35]
	v_mfma_f32_32x32x16_bf16 v[4:19], v[92:95], v[108:111], v[4:19]
	v_mfma_f32_32x32x16_bf16 v[20:35], v[80:83], v[112:115], v[20:35]
	v_mfma_f32_32x32x16_bf16 v[4:19], v[96:99], v[112:115], v[4:19]
	s_add_u32 s28, s28, 4
	s_addc_u32 s29, s29, 0
	v_lshl_add_u64 v[162:163], v[162:163], 0, s[38:39]
	s_cmp_eq_u32 s35, 63
	s_barrier
	s_cbranch_scc0 .LBB0_490
	s_waitcnt vmcnt(32)
	v_add_u32_e32 v82, v157, v155
	v_cvt_pk_bf16_f32 v52, v52, v53
	v_cvt_pk_bf16_f32 v53, v54, v55
	v_cvt_pk_bf16_f32 v54, v56, v57
	v_cvt_pk_bf16_f32 v57, v62, v63
	v_cvt_pk_bf16_f32 v62, v8, v9
	v_add_u32_e32 v8, 0xe800, v82
	v_cvt_pk_bf16_f32 v56, v60, v61
	v_cvt_pk_bf16_f32 v36, v36, v37
	v_cvt_pk_bf16_f32 v37, v38, v39
	v_cvt_pk_bf16_f32 v38, v40, v41
	v_cvt_pk_bf16_f32 v39, v42, v43
	v_cvt_pk_bf16_f32 v40, v44, v45
	v_cvt_pk_bf16_f32 v41, v46, v47
	v_cvt_pk_bf16_f32 v42, v48, v49
	v_cvt_pk_bf16_f32 v43, v50, v51
	v_cvt_pk_bf16_f32 v44, v20, v21
	v_cvt_pk_bf16_f32 v45, v22, v23
	v_cvt_pk_bf16_f32 v46, v24, v25
	v_cvt_pk_bf16_f32 v47, v26, v27
	v_cvt_pk_bf16_f32 v48, v28, v29
	v_cvt_pk_bf16_f32 v49, v30, v31
	v_cvt_pk_bf16_f32 v50, v32, v33
	v_cvt_pk_bf16_f32 v51, v34, v35
	v_cvt_pk_bf16_f32 v60, v4, v5
	v_cvt_pk_bf16_f32 v61, v6, v7
	ds_read2_b64 v[4:7], v8 offset0:64 offset1:66
	ds_read2_b64 v[20:23], v8 offset0:68 offset1:70
	ds_read2_b64 v[24:27], v8 offset0:72 offset1:74
	ds_read2_b64 v[28:31], v8 offset0:76 offset1:78
	ds_read2_b64 v[32:35], v8 offset0:80 offset1:82
	ds_read2_b64 v[68:71], v8 offset0:84 offset1:86
	ds_read2_b64 v[72:75], v8 offset0:88 offset1:90
	ds_read2_b64 v[78:81], v8 offset0:92 offset1:94
	s_add_u32 s24, s6, s24
	s_addc_u32 s25, s7, s25
	s_add_u32 s24, s24, s9
	s_addc_u32 s25, s25, 0
	v_lshl_add_u64 v[76:77], v[160:161], 2, s[24:25]
	v_cvt_pk_bf16_f32 v55, v58, v59
	v_cvt_pk_bf16_f32 v58, v64, v65
	v_cvt_pk_bf16_f32 v59, v66, v67
	v_cvt_pk_bf16_f32 v63, v10, v11
	v_cvt_pk_bf16_f32 v64, v12, v13
	v_cvt_pk_bf16_f32 v65, v14, v15
	v_cvt_pk_bf16_f32 v66, v16, v17
	v_cvt_pk_bf16_f32 v67, v18, v19
	s_waitcnt lgkmcnt(7)
	v_mfma_f32_32x32x16_bf16 v[4:19], v[4:7], v[52:55], 0
	s_waitcnt lgkmcnt(6)
	v_mfma_f32_32x32x16_bf16 v[4:19], v[20:23], v[56:59], v[4:19]
	s_waitcnt lgkmcnt(5)
	v_mfma_f32_32x32x16_bf16 v[4:19], v[24:27], v[36:39], v[4:19]
	s_waitcnt lgkmcnt(4)
	v_mfma_f32_32x32x16_bf16 v[4:19], v[28:31], v[40:43], v[4:19]
	s_waitcnt lgkmcnt(3)
	v_mfma_f32_32x32x16_bf16 v[4:19], v[32:35], v[44:47], v[4:19]
	s_waitcnt lgkmcnt(2)
	v_mfma_f32_32x32x16_bf16 v[4:19], v[68:71], v[48:51], v[4:19]
	s_waitcnt lgkmcnt(1)
	v_mfma_f32_32x32x16_bf16 v[4:19], v[72:75], v[60:63], v[4:19]
	s_waitcnt lgkmcnt(0)
	v_mfma_f32_32x32x16_bf16 v[4:19], v[78:81], v[64:67], v[4:19]
	v_add_u32_e32 v20, 0x2100, v82
	v_add_u32_e32 v24, 0xe800, v20
	ds_read2_b64 v[20:23], v24 offset0:64 offset1:66
	ds_read2_b64 v[68:71], v24 offset0:68 offset1:70
	ds_read2_b64 v[72:75], v24 offset0:72 offset1:74
	ds_read2_b64 v[78:81], v24 offset0:76 offset1:78
	ds_read2_b64 v[82:85], v24 offset0:80 offset1:82
	ds_read2_b64 v[86:89], v24 offset0:84 offset1:86
	ds_read2_b64 v[90:93], v24 offset0:88 offset1:90
	ds_read2_b64 v[94:97], v24 offset0:92 offset1:94
	s_waitcnt lgkmcnt(7)
	v_mfma_f32_32x32x16_bf16 v[20:35], v[20:23], v[52:55], 0
	s_waitcnt lgkmcnt(6)
	v_mfma_f32_32x32x16_bf16 v[20:35], v[68:71], v[56:59], v[20:35]
	s_waitcnt lgkmcnt(5)
	v_mfma_f32_32x32x16_bf16 v[20:35], v[72:75], v[36:39], v[20:35]
	s_waitcnt lgkmcnt(4)
	v_mfma_f32_32x32x16_bf16 v[20:35], v[78:81], v[40:43], v[20:35]
	s_waitcnt lgkmcnt(3)
	v_mfma_f32_32x32x16_bf16 v[20:35], v[82:85], v[44:47], v[20:35]
	s_waitcnt lgkmcnt(2)
	v_mfma_f32_32x32x16_bf16 v[20:35], v[86:89], v[48:51], v[20:35]
	s_waitcnt lgkmcnt(1)
	v_mfma_f32_32x32x16_bf16 v[20:35], v[90:93], v[60:63], v[20:35]
	s_waitcnt lgkmcnt(0)
	v_mfma_f32_32x32x16_bf16 v[20:35], v[94:97], v[64:67], v[20:35]
	v_add_f32_e64 v4, v166, -v4
	v_add_f32_e64 v5, v167, -v5
	v_add_f32_e64 v6, v164, -v6
	v_add_f32_e64 v7, v165, -v7
	v_add_f32_e64 v8, v168, -v8
	v_add_f32_e64 v9, v169, -v9
	v_pk_add_f32 v[10:11], v[170:171], v[10:11] neg_lo:[0,1] neg_hi:[0,1]
	v_pk_add_f32 v[12:13], v[180:181], v[12:13] neg_lo:[0,1] neg_hi:[0,1]
	v_pk_add_f32 v[14:15], v[194:195], v[14:15] neg_lo:[0,1] neg_hi:[0,1]
	v_pk_add_f32 v[16:17], v[196:197], v[16:17] neg_lo:[0,1] neg_hi:[0,1]
	v_pk_add_f32 v[18:19], v[198:199], v[18:19] neg_lo:[0,1] neg_hi:[0,1]
	v_cvt_pk_bf16_f32 v68, v4, v5
	v_cvt_pk_bf16_f32 v69, v6, v7
	v_pk_add_f32 v[4:5], v[172:173], v[20:21] neg_lo:[0,1] neg_hi:[0,1]
	v_pk_add_f32 v[6:7], v[174:175], v[22:23] neg_lo:[0,1] neg_hi:[0,1]
	v_add3_u32 v98, s31, v149, v155
	v_cvt_pk_bf16_f32 v70, v8, v9
	v_cvt_pk_bf16_f32 v71, v10, v11
	v_cvt_pk_bf16_f32 v72, v12, v13
	v_cvt_pk_bf16_f32 v73, v14, v15
	v_cvt_pk_bf16_f32 v74, v16, v17
	v_cvt_pk_bf16_f32 v75, v18, v19
	v_pk_add_f32 v[8:9], v[176:177], v[24:25] neg_lo:[0,1] neg_hi:[0,1]
	v_pk_add_f32 v[10:11], v[178:179], v[26:27] neg_lo:[0,1] neg_hi:[0,1]
	v_pk_add_f32 v[12:13], v[202:203], v[28:29] neg_lo:[0,1] neg_hi:[0,1]
	v_pk_add_f32 v[14:15], v[204:205], v[30:31] neg_lo:[0,1] neg_hi:[0,1]
	v_pk_add_f32 v[16:17], v[206:207], v[32:33] neg_lo:[0,1] neg_hi:[0,1]
	v_pk_add_f32 v[18:19], v[208:209], v[34:35] neg_lo:[0,1] neg_hi:[0,1]
	v_cvt_pk_bf16_f32 v78, v4, v5
	v_cvt_pk_bf16_f32 v79, v6, v7
	ds_read2_b64 v[4:7], v98 offset1:2
	ds_read2_b64 v[20:23], v98 offset0:4 offset1:6
	ds_read2_b64 v[24:27], v98 offset0:8 offset1:10
	ds_read2_b64 v[28:31], v98 offset0:12 offset1:14
	ds_read2_b64 v[32:35], v98 offset0:16 offset1:18
	ds_read2_b64 v[82:85], v98 offset0:20 offset1:22
	ds_read2_b64 v[86:89], v98 offset0:24 offset1:26
	ds_read2_b64 v[90:93], v98 offset0:28 offset1:30
	v_cvt_pk_bf16_f32 v80, v8, v9
	v_cvt_pk_bf16_f32 v81, v10, v11
	v_cvt_pk_bf16_f32 v94, v12, v13
	v_cvt_pk_bf16_f32 v95, v14, v15
	v_cvt_pk_bf16_f32 v96, v16, v17
	v_cvt_pk_bf16_f32 v97, v18, v19
	s_waitcnt lgkmcnt(7)
	v_mfma_f32_32x32x16_bf16 v[4:19], v[4:7], v[52:55], 0
	s_waitcnt lgkmcnt(6)
	v_mfma_f32_32x32x16_bf16 v[4:19], v[20:23], v[56:59], v[4:19]
	s_waitcnt lgkmcnt(5)
	v_mfma_f32_32x32x16_bf16 v[4:19], v[24:27], v[36:39], v[4:19]
	s_waitcnt lgkmcnt(4)
	v_mfma_f32_32x32x16_bf16 v[4:19], v[28:31], v[40:43], v[4:19]
	s_waitcnt lgkmcnt(3)
	v_mfma_f32_32x32x16_bf16 v[4:19], v[32:35], v[44:47], v[4:19]
	s_waitcnt lgkmcnt(2)
	v_mfma_f32_32x32x16_bf16 v[4:19], v[82:85], v[48:51], v[4:19]
	s_waitcnt lgkmcnt(1)
	v_mfma_f32_32x32x16_bf16 v[4:19], v[86:89], v[60:63], v[4:19]
	s_waitcnt lgkmcnt(0)
	v_mfma_f32_32x32x16_bf16 v[4:19], v[90:93], v[64:67], v[4:19]
	v_add_u32_e32 v24, 0x2000, v98
	ds_read2_b64 v[20:23], v24 offset0:32 offset1:34
	ds_read2_b64 v[82:85], v24 offset0:36 offset1:38
	ds_read2_b64 v[86:89], v24 offset0:40 offset1:42
	ds_read2_b64 v[90:93], v24 offset0:44 offset1:46
	ds_read2_b64 v[98:101], v24 offset0:48 offset1:50
	ds_read2_b64 v[102:105], v24 offset0:52 offset1:54
	ds_read2_b64 v[106:109], v24 offset0:56 offset1:58
	ds_read2_b64 v[110:113], v24 offset0:60 offset1:62
	s_waitcnt lgkmcnt(7)
	v_mfma_f32_32x32x16_bf16 v[20:35], v[20:23], v[52:55], 0
	s_waitcnt lgkmcnt(6)
	v_mfma_f32_32x32x16_bf16 v[20:35], v[82:85], v[56:59], v[20:35]
	s_waitcnt lgkmcnt(5)
	v_mfma_f32_32x32x16_bf16 v[20:35], v[86:89], v[36:39], v[20:35]
	s_waitcnt lgkmcnt(4)
	v_mfma_f32_32x32x16_bf16 v[20:35], v[90:93], v[40:43], v[20:35]
	s_waitcnt lgkmcnt(3)
	v_mfma_f32_32x32x16_bf16 v[20:35], v[98:101], v[44:47], v[20:35]
	s_waitcnt lgkmcnt(2)
	v_mfma_f32_32x32x16_bf16 v[20:35], v[102:105], v[48:51], v[20:35]
	s_waitcnt lgkmcnt(1)
	v_mfma_f32_32x32x16_bf16 v[20:35], v[106:109], v[60:63], v[20:35]
	s_waitcnt lgkmcnt(0)
	v_mfma_f32_32x32x16_bf16 v[20:35], v[110:113], v[64:67], v[20:35]
	v_add3_u32 v52, s33, v149, v153
	v_add_u32_e32 v64, 0x1000, v52
	ds_read2_b64 v[36:39], v52 offset1:2
	ds_read2_b64 v[40:43], v52 offset0:4 offset1:6
	ds_read2_b64 v[44:47], v52 offset0:8 offset1:10
	ds_read2_b64 v[48:51], v52 offset0:12 offset1:14
	ds_read2_b64 v[52:55], v64 offset0:32 offset1:34
	ds_read2_b64 v[56:59], v64 offset0:36 offset1:38
	ds_read2_b64 v[60:63], v64 offset0:40 offset1:42
	ds_read2_b64 v[64:67], v64 offset0:44 offset1:46
	s_waitcnt lgkmcnt(7)
	v_mfma_f32_32x32x16_bf16 v[4:19], v[36:39], v[68:71], v[4:19]
	s_waitcnt lgkmcnt(3)
	v_mfma_f32_32x32x16_bf16 v[20:35], v[52:55], v[68:71], v[20:35]
	v_mfma_f32_32x32x16_bf16 v[4:19], v[40:43], v[72:75], v[4:19]
	s_waitcnt lgkmcnt(2)
	v_mfma_f32_32x32x16_bf16 v[20:35], v[56:59], v[72:75], v[20:35]
	v_mfma_f32_32x32x16_bf16 v[4:19], v[44:47], v[78:81], v[4:19]
	s_waitcnt lgkmcnt(1)
	v_mfma_f32_32x32x16_bf16 v[20:35], v[60:63], v[78:81], v[20:35]
	v_mfma_f32_32x32x16_bf16 v[4:19], v[48:51], v[94:97], v[4:19]
	s_waitcnt lgkmcnt(0)
	v_mfma_f32_32x32x16_bf16 v[20:35], v[64:67], v[94:97], v[20:35]
	v_lshl_add_u64 v[36:37], v[76:77], 0, v[2:3]
	s_mov_b32 s9, 0x479e0000
	v_add_co_u32_e32 v38, vcc, s9, v36
	s_mov_b32 s9, 0x479e1000
	s_nop 0
	v_addc_co_u32_e32 v39, vcc, 0, v37, vcc
	s_nop 3
	global_store_dword v[38:39], v4, off
	global_store_dword v[38:39], v5, off offset:2048
	v_add_co_u32_e32 v4, vcc, s9, v36
	s_mov_b32 s9, 0x479e4000
	s_nop 0
	v_addc_co_u32_e32 v5, vcc, 0, v37, vcc
	global_store_dword v[4:5], v6, off
	global_store_dword v[4:5], v7, off offset:2048
	v_add_co_u32_e32 v4, vcc, s9, v36
	s_mov_b32 s9, 0x479e5000
	s_nop 0
	v_addc_co_u32_e32 v5, vcc, 0, v37, vcc
	global_store_dword v[4:5], v8, off
	global_store_dword v[4:5], v9, off offset:2048
	v_add_co_u32_e32 v4, vcc, s9, v36
	s_mov_b32 s9, 0x479e8000
	s_nop 0
	v_addc_co_u32_e32 v5, vcc, 0, v37, vcc
	global_store_dword v[4:5], v10, off
	global_store_dword v[4:5], v11, off offset:2048
	v_add_co_u32_e32 v4, vcc, s9, v36
	s_mov_b32 s9, 0x479e9000
	s_nop 0
	v_addc_co_u32_e32 v5, vcc, 0, v37, vcc
	global_store_dword v[4:5], v12, off
	global_store_dword v[4:5], v13, off offset:2048
	v_add_co_u32_e32 v4, vcc, s9, v36
	s_mov_b32 s9, 0x479ec000
	s_nop 0
	v_addc_co_u32_e32 v5, vcc, 0, v37, vcc
	global_store_dword v[4:5], v14, off
	global_store_dword v[4:5], v15, off offset:2048
	v_add_co_u32_e32 v4, vcc, s9, v36
	s_mov_b32 s9, 0x479ed000
	s_nop 0
	v_addc_co_u32_e32 v5, vcc, 0, v37, vcc
	global_store_dword v[4:5], v16, off
	global_store_dword v[4:5], v17, off offset:2048
	v_add_co_u32_e32 v4, vcc, s9, v36
	s_mov_b32 s9, 0x479f0000
	s_nop 0
	v_addc_co_u32_e32 v5, vcc, 0, v37, vcc
	global_store_dword v[4:5], v18, off
	global_store_dword v[4:5], v19, off offset:2048
	v_add_co_u32_e32 v4, vcc, s9, v36
	s_mov_b32 s9, 0x479f1000
	s_nop 0
	v_addc_co_u32_e32 v5, vcc, 0, v37, vcc
	global_store_dword v[4:5], v20, off
	global_store_dword v[4:5], v21, off offset:2048
	v_add_co_u32_e32 v4, vcc, s9, v36
	s_mov_b32 s9, 0x479f4000
	s_nop 0
	v_addc_co_u32_e32 v5, vcc, 0, v37, vcc
	global_store_dword v[4:5], v22, off
	global_store_dword v[4:5], v23, off offset:2048
	v_add_co_u32_e32 v4, vcc, s9, v36
	s_mov_b32 s9, 0x479f5000
	s_nop 0
	v_addc_co_u32_e32 v5, vcc, 0, v37, vcc
	global_store_dword v[4:5], v24, off
	global_store_dword v[4:5], v25, off offset:2048
	v_add_co_u32_e32 v4, vcc, s9, v36
	s_mov_b32 s9, 0x479f8000
	s_nop 0
	v_addc_co_u32_e32 v5, vcc, 0, v37, vcc
	global_store_dword v[4:5], v26, off
	global_store_dword v[4:5], v27, off offset:2048
	v_add_co_u32_e32 v4, vcc, s9, v36
	s_mov_b32 s9, 0x479f9000
	s_nop 0
	v_addc_co_u32_e32 v5, vcc, 0, v37, vcc
	global_store_dword v[4:5], v28, off
	global_store_dword v[4:5], v29, off offset:2048
	v_add_co_u32_e32 v4, vcc, s9, v36
	s_mov_b32 s9, 0x479fc000
	s_nop 0
	v_addc_co_u32_e32 v5, vcc, 0, v37, vcc
	global_store_dword v[4:5], v30, off
	global_store_dword v[4:5], v31, off offset:2048
	v_add_co_u32_e32 v4, vcc, s9, v36
	s_nop 1
	v_addc_co_u32_e32 v5, vcc, 0, v37, vcc
	global_store_dword v[4:5], v32, off
	global_store_dword v[4:5], v33, off offset:2048
	v_add_co_u32_e32 v4, vcc, 0x479fd000, v36
	s_nop 1
	v_addc_co_u32_e32 v5, vcc, 0, v37, vcc
	global_store_dword v[4:5], v34, off
	global_store_dword v[4:5], v35, off offset:2048
	s_mov_b64 s[28:29], 0
	s_waitcnt lgkmcnt(0)
	s_barrier

.LBB0_522:
	v_add_u32_e32 v2, s14, v220
	v_mad_i64_i32 v[4:5], s[12:13], v2, s24, v[200:201]
	v_add_u32_e32 v2, s14, v219
	v_mad_i64_i32 v[6:7], s[12:13], v2, s24, v[200:201]
	v_add_u32_e32 v2, s14, v218
	global_load_dwordx4 v[8:11], v[204:205], off
	global_load_dwordx4 v[114:117], v[4:5], off
	global_load_dwordx4 v[12:15], v[6:7], off
	s_nop 0
	global_load_dwordx4 v[4:7], v[202:203], off
	v_lshl_add_u64 v[16:17], v[2:3], 2, s[10:11]
	global_load_dword v2, v[16:17], off
	s_cmp_gt_i32 s14, s19
	s_cbranch_scc1 .LBB0_528
	s_bitcmp1_b32 s20, 0
	s_cselect_b32 s12, 0, 0x8900
	s_add_i32 s12, s72, s12
	v_add3_u32 v16, s12, v217, v196
	ds_read_b128 v[82:85], v16
	ds_read_b128 v[118:121], v16 offset:32
	ds_read_b128 v[86:89], v16 offset:8704
	ds_read_b128 v[122:125], v16 offset:8736
	ds_read_b128 v[126:129], v16 offset:64
	ds_read_b128 v[130:133], v16 offset:96
	ds_read_b128 v[134:137], v16 offset:8768
	ds_read_b128 v[138:141], v16 offset:8800
	s_waitcnt lgkmcnt(0)
	v_mfma_f32_32x32x16_bf16 v[98:113], v[82:85], v[174:177], 0
	v_mfma_f32_32x32x16_bf16 v[82:97], v[86:89], v[174:177], 0
	v_mfma_f32_32x32x16_bf16 v[98:113], v[118:121], v[170:173], v[98:113]
	v_mfma_f32_32x32x16_bf16 v[82:97], v[122:125], v[170:173], v[82:97]
	v_mfma_f32_32x32x16_bf16 v[98:113], v[126:129], v[166:169], v[98:113]
	v_mfma_f32_32x32x16_bf16 v[82:97], v[134:137], v[166:169], v[82:97]
	v_mfma_f32_32x32x16_bf16 v[98:113], v[130:133], v[162:165], v[98:113]
	v_mfma_f32_32x32x16_bf16 v[82:97], v[138:141], v[162:165], v[82:97]
	ds_read_b128 v[118:121], v16 offset:128
	ds_read_b128 v[122:125], v16 offset:160
	ds_read_b128 v[126:129], v16 offset:8832
	ds_read_b128 v[130:133], v16 offset:8864
	ds_read_b128 v[134:137], v16 offset:192
	ds_read_b128 v[142:145], v16 offset:224
	ds_read_b128 v[138:141], v16 offset:8896
	ds_read_b128 v[182:185], v16 offset:8928
	s_waitcnt lgkmcnt(0)
	v_mfma_f32_32x32x16_bf16 v[98:113], v[118:121], v[158:161], v[98:113]
	v_add_u32_e32 v16, s12, v199
	v_add_u32_e32 v221, v16, v197
	v_add_u32_e32 v16, 0x4000, v221
	v_mfma_f32_32x32x16_bf16 v[82:97], v[126:129], v[158:161], v[82:97]
	v_mfma_f32_32x32x16_bf16 v[98:113], v[122:125], v[154:157], v[98:113]
	v_mfma_f32_32x32x16_bf16 v[82:97], v[130:133], v[154:157], v[82:97]
	v_mfma_f32_32x32x16_bf16 v[98:113], v[134:137], v[150:153], v[98:113]
	v_mfma_f32_32x32x16_bf16 v[82:97], v[138:141], v[150:153], v[82:97]
	ds_read2_b64 v[178:181], v16 offset0:128 offset1:130
	ds_read2_b64 v[138:141], v16 offset0:132 offset1:134
	v_mfma_f32_32x32x16_bf16 v[98:113], v[142:145], v[146:149], v[98:113]
	ds_read2_b64 v[142:145], v16 offset0:136 offset1:138
	ds_read2_b64 v[134:137], v16 offset0:140 offset1:142
	v_add_u32_e32 v16, 0x5000, v221
	ds_read2_b64 v[130:133], v16 offset0:160 offset1:162
	ds_read2_b64 v[126:129], v16 offset0:164 offset1:166
	ds_read2_b64 v[122:125], v16 offset0:168 offset1:170
	ds_read2_b64 v[118:121], v16 offset0:172 offset1:174
	v_mfma_f32_32x32x16_bf16 v[82:97], v[182:185], v[146:149], v[82:97]
	v_lshl_add_u32 v16, v1, 2, s12
	ds_read_b128 v[182:185], v16 offset:34816
	ds_read_b128 v[186:189], v16 offset:34848
	ds_read_b128 v[222:225], v16 offset:34944
	ds_read_b128 v[232:235], v16 offset:34976
	ds_read_b128 v[236:239], v16 offset:34880
	ds_read_b128 v[242:245], v16 offset:34912
	ds_read_b128 v[246:249], v16 offset:35008
	ds_read_b128 v[190:193], v16 offset:35040
	s_add_i32 s13, s14, 63
	s_waitcnt lgkmcnt(0)
	v_xor_b32_e32 v185, 0x80000000, v185
	v_xor_b32_e32 v184, 0x80000000, v184
	v_xor_b32_e32 v17, 0x80000000, v245
	v_xor_b32_e32 v16, 0x80000000, v244
	s_mov_b32 s12, 0x3e0293ee
	v_xor_b32_e32 v189, 0x80000000, v189
	v_xor_b32_e32 v188, 0x80000000, v188
	v_xor_b32_e32 v239, 0x80000000, v239
	v_xor_b32_e32 v238, 0x80000000, v238
	v_fma_f32 v206, v102, s12, -v186
	v_fma_f32 v207, v103, s12, -v187
	v_fma_f32 v16, v112, s12, v16
	v_fma_f32 v17, v113, s12, v17
	v_fma_f32 v100, v100, s12, v184
	v_fma_f32 v101, v101, s12, v185
	v_fma_f32 v98, v98, s12, -v182
	v_fma_f32 v99, v99, s12, -v183
	v_xor_b32_e32 v113, 0x80000000, v225
	v_xor_b32_e32 v112, 0x80000000, v224
	v_xor_b32_e32 v183, 0x80000000, v235
	v_xor_b32_e32 v182, 0x80000000, v234
	v_xor_b32_e32 v185, 0x80000000, v249
	v_xor_b32_e32 v184, 0x80000000, v248
	v_xor_b32_e32 v187, 0x80000000, v193
	v_xor_b32_e32 v186, 0x80000000, v192
	v_fma_f32 v110, v110, s12, -v242
	v_fma_f32 v111, v111, s12, -v243
	v_fma_f32 v106, v106, s12, -v236
	v_fma_f32 v107, v107, s12, -v237
	v_fma_f32 v102, v108, s12, v238
	v_fma_f32 v103, v109, s12, v239
	v_fma_f32 v104, v104, s12, v188
	v_fma_f32 v105, v105, s12, v189
	v_fma_f32 v94, v94, s12, -v190
	v_fma_f32 v95, v95, s12, -v191
	v_fma_f32 v90, v90, s12, -v246
	v_fma_f32 v91, v91, s12, -v247
	v_fma_f32 v108, v86, s12, -v232
	v_fma_f32 v109, v87, s12, -v233
	v_fma_f32 v86, v96, s12, v186
	v_fma_f32 v87, v97, s12, v187
	v_fma_f32 v92, v92, s12, v184
	v_fma_f32 v93, v93, s12, v185
	v_fma_f32 v88, v88, s12, v182
	v_fma_f32 v89, v89, s12, v183
	v_fma_f32 v84, v84, s12, v112
	v_fma_f32 v85, v85, s12, v113
	s_cmp_le_i32 s13, s18
	v_fma_f32 v82, v82, s12, -v222
	v_fma_f32 v83, v83, s12, -v223
	s_cbranch_scc1 .LBB0_525
	v_add_u32_e32 v96, s14, v1
	v_add_u32_e32 v97, 32, v96
	v_cmp_le_i32_e32 vcc, v97, v211
	v_add_u32_e32 v97, 33, v96
	s_nop 0
	v_cndmask_b32_e32 v82, v229, v82, vcc
	v_cmp_lt_i32_e32 vcc, v96, v211
	s_nop 1
	v_cndmask_b32_e32 v99, v229, v99, vcc
	v_cmp_le_i32_e32 vcc, v96, v211
	s_nop 1
	v_cndmask_b32_e32 v98, v229, v98, vcc
	v_cmp_le_i32_e32 vcc, v97, v211
	v_add_u32_e32 v97, 2, v96
	s_nop 0
	v_cndmask_b32_e32 v83, v229, v83, vcc
	v_cmp_le_i32_e32 vcc, v97, v211
	v_add_u32_e32 v97, 34, v96
	s_nop 0
	v_cndmask_b32_e32 v100, v229, v100, vcc
	v_cmp_le_i32_e32 vcc, v97, v211
	v_add_u32_e32 v97, 3, v96
	s_nop 0
	v_cndmask_b32_e32 v84, v229, v84, vcc
	v_cmp_le_i32_e32 vcc, v97, v211
	v_add_u32_e32 v97, 35, v96
	s_nop 0
	v_cndmask_b32_e32 v101, v229, v101, vcc
	v_cmp_le_i32_e32 vcc, v97, v211
	v_add_u32_e32 v97, 8, v96
	s_nop 0
	v_cndmask_b32_e32 v85, v229, v85, vcc
	v_cmp_le_i32_e32 vcc, v97, v211
	v_add_u32_e32 v97, 40, v96
	s_nop 0
	v_cndmask_b32_e32 v206, v229, v206, vcc
	v_cmp_le_i32_e32 vcc, v97, v211
	v_add_u32_e32 v97, 9, v96
	s_nop 0
	v_cndmask_b32_e32 v108, v229, v108, vcc
	v_cmp_le_i32_e32 vcc, v97, v211
	v_add_u32_e32 v97, 41, v96
	s_nop 0
	v_cndmask_b32_e32 v207, v229, v207, vcc
	v_cmp_le_i32_e32 vcc, v97, v211
	v_add_u32_e32 v97, 10, v96
	s_nop 0
	v_cndmask_b32_e32 v109, v229, v109, vcc
	v_cmp_le_i32_e32 vcc, v97, v211
	v_add_u32_e32 v97, 42, v96
	s_nop 0
	v_cndmask_b32_e32 v104, v229, v104, vcc
	v_cmp_le_i32_e32 vcc, v97, v211
	v_add_u32_e32 v97, 11, v96
	s_nop 0
	v_cndmask_b32_e32 v88, v229, v88, vcc
	v_cmp_le_i32_e32 vcc, v97, v211
	v_add_u32_e32 v97, 43, v96
	s_nop 0
	v_cndmask_b32_e32 v105, v229, v105, vcc
	v_cmp_le_i32_e32 vcc, v97, v211
	v_add_u32_e32 v97, 16, v96
	s_nop 0
	v_cndmask_b32_e32 v89, v229, v89, vcc
	v_cmp_le_i32_e32 vcc, v97, v211
	v_add_u32_e32 v97, 48, v96
	s_nop 0
	v_cndmask_b32_e32 v106, v229, v106, vcc
	v_cmp_le_i32_e32 vcc, v97, v211
	v_add_u32_e32 v97, 17, v96
	s_nop 0
	v_cndmask_b32_e32 v90, v229, v90, vcc
	v_cmp_le_i32_e32 vcc, v97, v211
	v_add_u32_e32 v97, 49, v96
	s_nop 0
	v_cndmask_b32_e32 v107, v229, v107, vcc
	v_cmp_le_i32_e32 vcc, v97, v211
	v_add_u32_e32 v97, 18, v96
	s_nop 0
	v_cndmask_b32_e32 v91, v229, v91, vcc
	v_cmp_le_i32_e32 vcc, v97, v211
	v_add_u32_e32 v97, 50, v96
	s_nop 0
	v_cndmask_b32_e32 v102, v229, v102, vcc
	v_cmp_le_i32_e32 vcc, v97, v211
	v_add_u32_e32 v97, 19, v96
	s_nop 0
	v_cndmask_b32_e32 v92, v229, v92, vcc
	v_cmp_le_i32_e32 vcc, v97, v211
	v_add_u32_e32 v97, 51, v96
	s_nop 0
	v_cndmask_b32_e32 v103, v229, v103, vcc
	v_cmp_le_i32_e32 vcc, v97, v211
	v_add_u32_e32 v97, 24, v96
	s_nop 0
	v_cndmask_b32_e32 v93, v229, v93, vcc
	v_cmp_le_i32_e32 vcc, v97, v211
	v_add_u32_e32 v97, 56, v96
	s_nop 0
	v_cndmask_b32_e32 v110, v229, v110, vcc
	v_cmp_le_i32_e32 vcc, v97, v211
	v_add_u32_e32 v97, 25, v96
	s_nop 0
	v_cndmask_b32_e32 v94, v229, v94, vcc
	v_cmp_le_i32_e32 vcc, v97, v211
	v_add_u32_e32 v97, 57, v96
	s_nop 0
	v_cndmask_b32_e32 v111, v229, v111, vcc
	v_cmp_le_i32_e32 vcc, v97, v211
	v_add_u32_e32 v97, 26, v96
	s_nop 0
	v_cndmask_b32_e32 v95, v229, v95, vcc
	v_cmp_le_i32_e32 vcc, v97, v211
	v_add_u32_e32 v97, 58, v96
	s_nop 0
	v_cndmask_b32_e32 v16, v229, v16, vcc
	v_cmp_le_i32_e32 vcc, v97, v211
	v_add_u32_e32 v97, 27, v96
	v_add_u32_e32 v96, 59, v96
	v_cndmask_b32_e32 v86, v229, v86, vcc
	v_cmp_le_i32_e32 vcc, v97, v211
	s_nop 1
	v_cndmask_b32_e32 v17, v229, v17, vcc
	v_cmp_le_i32_e32 vcc, v96, v211
	s_nop 1
	v_cndmask_b32_e32 v87, v229, v87, vcc
.LBB0_525:
	v_max3_f32 v96, v229, v98, v82
	v_max3_f32 v97, v229, v99, v83
	s_nop 0
	v_max3_f32 v96, v96, v100, v84
	v_max3_f32 v97, v97, v101, v85
	s_nop 0
	v_max3_f32 v96, v96, v206, v108
	v_max3_f32 v97, v97, v207, v109
	s_nop 0
	v_max3_f32 v96, v96, v104, v88
	v_max3_f32 v97, v97, v105, v89
	s_nop 0
	v_max3_f32 v96, v96, v106, v90
	v_max3_f32 v97, v97, v107, v91
	s_nop 0
	v_max3_f32 v96, v96, v102, v92
	v_max3_f32 v97, v97, v103, v93
	s_nop 0
	v_max3_f32 v96, v96, v110, v94
	v_max3_f32 v97, v97, v111, v95
	s_nop 0
	v_max3_f32 v96, v96, v16, v86
	v_max3_f32 v97, v97, v17, v87
	s_nop 0
	v_max_f32 v96, v96, v97
	v_mbcnt_hi_u32_b32 v97, -1, v251
	v_and_b32_e32 v113, 64, v97
	v_xor_b32_e32 v112, 32, v97
	v_add_u32_e32 v113, 64, v113
	v_cmp_lt_i32_e32 vcc, v112, v113
	s_nop 1
	v_cndmask_b32_e32 v97, v97, v112, vcc
	v_lshlrev_b32_e32 v97, 2, v97
	ds_bpermute_b32 v97, v97, v96
	s_waitcnt lgkmcnt(0)
	v_max3_f32 v96, v212, v96, v97
	v_cmp_gt_f32_e32 vcc, v96, v212
	s_cbranch_vccz .LBB0_527
	v_sub_f32_e32 v97, v212, v96
	v_exp_f32_e32 v112, v97
	v_mov_b32_e32 v212, v96
	v_mul_f32_e32 v80, v80, v112
	v_mul_f32_e32 v81, v81, v112
	v_mul_f32_e32 v78, v78, v112
	v_mul_f32_e32 v79, v79, v112
	v_mul_f32_e32 v76, v76, v112
	v_mul_f32_e32 v77, v77, v112
	v_mul_f32_e32 v74, v74, v112
	v_mul_f32_e32 v75, v75, v112
	v_mul_f32_e32 v72, v72, v112
	v_mul_f32_e32 v73, v73, v112
	v_mul_f32_e32 v70, v70, v112
	v_mul_f32_e32 v71, v71, v112
	v_mul_f32_e32 v68, v68, v112
	v_mul_f32_e32 v69, v69, v112
	v_mul_f32_e32 v66, v66, v112
	v_mul_f32_e32 v67, v67, v112
	v_mul_f32_e32 v64, v64, v112
	v_mul_f32_e32 v65, v65, v112
	v_mul_f32_e32 v62, v62, v112
	v_mul_f32_e32 v63, v63, v112
	v_mul_f32_e32 v60, v60, v112
	v_mul_f32_e32 v61, v61, v112
	v_mul_f32_e32 v58, v58, v112
	v_mul_f32_e32 v59, v59, v112
	v_mul_f32_e32 v56, v56, v112
	v_mul_f32_e32 v57, v57, v112
	v_mul_f32_e32 v54, v54, v112
	v_mul_f32_e32 v55, v55, v112
	v_mul_f32_e32 v52, v52, v112
	v_mul_f32_e32 v53, v53, v112
	v_mul_f32_e32 v50, v50, v112
	v_mul_f32_e32 v51, v51, v112
	v_mul_f32_e32 v48, v48, v112
	v_mul_f32_e32 v49, v49, v112
	v_mul_f32_e32 v46, v46, v112
	v_mul_f32_e32 v47, v47, v112
	v_mul_f32_e32 v44, v44, v112
	v_mul_f32_e32 v45, v45, v112
	v_mul_f32_e32 v42, v42, v112
	v_mul_f32_e32 v43, v43, v112
	v_mul_f32_e32 v40, v40, v112
	v_mul_f32_e32 v41, v41, v112
	v_mul_f32_e32 v38, v38, v112
	v_mul_f32_e32 v39, v39, v112
	v_mul_f32_e32 v36, v36, v112
	v_mul_f32_e32 v37, v37, v112
	v_mul_f32_e32 v34, v34, v112
	v_mul_f32_e32 v35, v35, v112
	v_mul_f32_e32 v32, v32, v112
	v_mul_f32_e32 v33, v33, v112
	v_mul_f32_e32 v30, v30, v112
	v_mul_f32_e32 v31, v31, v112
	v_mul_f32_e32 v28, v28, v112
	v_mul_f32_e32 v29, v29, v112
	v_mul_f32_e32 v26, v26, v112
	v_mul_f32_e32 v27, v27, v112
	v_mul_f32_e32 v24, v24, v112
	v_mul_f32_e32 v25, v25, v112
	v_mul_f32_e32 v22, v22, v112
	v_mul_f32_e32 v23, v23, v112
	v_mul_f32_e32 v20, v20, v112
	v_mul_f32_e32 v21, v21, v112
	v_mul_f32_e32 v18, v18, v112
	v_mul_f32_e32 v19, v19, v112
	v_mul_f32_e32 v210, v210, v112
.LBB0_527:
	v_sub_f32_e32 v84, v84, v96
	v_sub_f32_e32 v83, v83, v96
	v_exp_f32_e32 v232, v84
	v_sub_f32_e32 v84, v101, v96
	v_sub_f32_e32 v88, v88, v96
	v_sub_f32_e32 v97, v98, v96
	v_exp_f32_e32 v223, v83
	v_sub_f32_e32 v83, v100, v96
	v_exp_f32_e32 v233, v84
	v_sub_f32_e32 v84, v85, v96
	v_sub_f32_e32 v98, v109, v96
	v_sub_f32_e32 v100, v104, v96
	v_exp_f32_e32 v109, v88
	v_sub_f32_e32 v88, v105, v96
	v_exp_f32_e32 v234, v84
	v_sub_f32_e32 v84, v206, v96
	v_exp_f32_e32 v101, v100
	v_exp_f32_e32 v100, v88
	v_sub_f32_e32 v88, v89, v96
	v_exp_f32_e32 v85, v84
	v_sub_f32_e32 v84, v108, v96
	v_exp_f32_e32 v108, v88
	v_sub_f32_e32 v88, v106, v96
	v_exp_f32_e32 v183, v88
	v_sub_f32_e32 v88, v90, v96
	v_exp_f32_e32 v185, v88
	v_sub_f32_e32 v88, v107, v96
	v_exp_f32_e32 v182, v88
	v_sub_f32_e32 v88, v91, v96
	v_exp_f32_e32 v184, v88
	v_sub_f32_e32 v88, v102, v96
	v_exp_f32_e32 v107, v88
	v_sub_f32_e32 v88, v92, v96
	v_exp_f32_e32 v187, v88
	v_sub_f32_e32 v88, v103, v96
	v_exp_f32_e32 v106, v88
	v_sub_f32_e32 v88, v93, v96
	v_exp_f32_e32 v186, v88
	v_sub_f32_e32 v88, v110, v96
	v_exp_f32_e32 v93, v88
	v_sub_f32_e32 v88, v94, v96
	v_exp_f32_e32 v103, v88
	v_sub_f32_e32 v88, v111, v96
	v_sub_f32_e32 v16, v16, v96
	v_exp_f32_e32 v92, v88
	v_sub_f32_e32 v88, v95, v96
	v_exp_f32_e32 v95, v16
	v_sub_f32_e32 v16, v86, v96
	v_sub_f32_e32 v82, v82, v96
	v_exp_f32_e32 v111, v16
	v_sub_f32_e32 v16, v17, v96
	v_exp_f32_e32 v222, v82
	v_sub_f32_e32 v82, v99, v96
	v_exp_f32_e32 v99, v84
	v_exp_f32_e32 v98, v98
	v_exp_f32_e32 v94, v16
	v_sub_f32_e32 v16, v87, v96
	v_exp_f32_e32 v97, v97
	v_exp_f32_e32 v82, v82
	v_exp_f32_e32 v102, v88
	v_exp_f32_e32 v110, v16
	v_sub_f32_e32 v84, v207, v96
	v_exp_f32_e32 v84, v84
	v_pk_mov_b32 v[88:89], v[98:99], v[98:99] op_sel:[1,0]
	v_pk_mov_b32 v[90:91], v[108:109], v[108:109] op_sel:[1,0]
	v_add_f32_e32 v224, v97, v222
	v_add_f32_e32 v225, v82, v223
	v_exp_f32_e32 v83, v83
	v_add_f32_e32 v190, v92, v102
	v_add_f32_e32 v191, v93, v103
	v_add_f32_e32 v192, v94, v110
	v_add_f32_e32 v193, v95, v111
	v_cvt_pk_bf16_f32 v82, v97, v82
	v_cvt_pk_bf16_f32 v88, v88, v89
	v_cvt_pk_bf16_f32 v89, v90, v91
	v_pk_mov_b32 v[90:91], v[182:183], v[182:183] op_sel:[1,0]
	v_pk_mov_b32 v[96:97], v[106:107], v[106:107] op_sel:[1,0]
	v_pk_mov_b32 v[92:93], v[92:93], v[92:93] op_sel:[1,0]
	v_pk_mov_b32 v[94:95], v[94:95], v[94:95] op_sel:[1,0]
	v_cvt_pk_bf16_f32 v90, v90, v91
	v_cvt_pk_bf16_f32 v91, v96, v97
	v_cvt_pk_bf16_f32 v92, v92, v93
	v_cvt_pk_bf16_f32 v93, v94, v95
	v_pk_mov_b32 v[94:95], v[184:185], v[184:185] op_sel:[1,0]
	v_pk_mov_b32 v[96:97], v[186:187], v[186:187] op_sel:[1,0]
	v_add_f32_e32 v104, v84, v98
	v_add_f32_e32 v105, v85, v99
	v_cvt_pk_bf16_f32 v94, v94, v95
	v_cvt_pk_bf16_f32 v95, v96, v97
	v_pk_mov_b32 v[96:97], v[102:103], v[102:103] op_sel:[1,0]
	v_pk_mov_b32 v[98:99], v[110:111], v[110:111] op_sel:[1,0]
	v_cvt_pk_bf16_f32 v96, v96, v97
	v_cvt_pk_bf16_f32 v97, v98, v99
	v_add_f32_e32 v98, 0, v224
	v_add_f32_e32 v206, v83, v232
	v_add_f32_e32 v98, v225, v98
	v_add_f32_e32 v207, v233, v234
	v_add_f32_e32 v98, v206, v98
	v_add_f32_e32 v98, v207, v98
	v_add_f32_e32 v98, v105, v98
	v_add_f32_e32 v112, v100, v108
	v_add_f32_e32 v113, v101, v109
	v_add_f32_e32 v98, v104, v98
	v_add_f32_e32 v98, v113, v98
	v_add_f32_e32 v16, v182, v184
	v_add_f32_e32 v17, v183, v185
	v_add_f32_e32 v98, v112, v98
	v_add_f32_e32 v17, v17, v98
	v_add_f32_e32 v188, v106, v186
	v_add_f32_e32 v189, v107, v187
	v_add_f32_e32 v16, v16, v17
	v_add_f32_e32 v16, v189, v16
	v_add_f32_e32 v16, v188, v16
	v_add_f32_e32 v16, v191, v16
	v_add_f32_e32 v16, v190, v16
	v_pk_mov_b32 v[84:85], v[84:85], v[84:85] op_sel:[1,0]
	v_pk_mov_b32 v[86:87], v[100:101], v[100:101] op_sel:[1,0]
	v_add_f32_e32 v16, v193, v16
	v_cvt_pk_bf16_f32 v83, v83, v233
	v_cvt_pk_bf16_f32 v84, v84, v85
	v_cvt_pk_bf16_f32 v85, v86, v87
	v_cvt_pk_bf16_f32 v86, v222, v223
	v_cvt_pk_bf16_f32 v87, v232, v234
	v_add_f32_e32 v16, v192, v16
	v_add_u32_e32 v17, 0x6000, v221
	ds_read2_b64 v[98:101], v17 offset0:192 offset1:194
	ds_read2_b64 v[102:105], v17 offset0:196 offset1:198
	ds_read2_b64 v[106:109], v17 offset0:200 offset1:202
	ds_read2_b64 v[110:113], v17 offset0:204 offset1:206
	v_add_u32_e32 v17, 0x7000, v221
	ds_read2_b64 v[182:185], v17 offset0:224 offset1:226
	ds_read2_b64 v[186:189], v17 offset0:228 offset1:230
	ds_read2_b64 v[190:193], v17 offset0:232 offset1:234
	ds_read2_b64 v[222:225], v17 offset0:236 offset1:238
	v_mfma_f32_32x32x16_bf16 v[66:81], v[178:181], v[82:85], v[66:81]
	v_mfma_f32_32x32x16_bf16 v[50:65], v[130:133], v[82:85], v[50:65]
	v_mfma_f32_32x32x16_bf16 v[66:81], v[138:141], v[90:93], v[66:81]
	v_mfma_f32_32x32x16_bf16 v[50:65], v[126:129], v[90:93], v[50:65]
	v_mfma_f32_32x32x16_bf16 v[66:81], v[142:145], v[86:89], v[66:81]
	v_mfma_f32_32x32x16_bf16 v[50:65], v[122:125], v[86:89], v[50:65]
	v_mfma_f32_32x32x16_bf16 v[66:81], v[134:137], v[94:97], v[66:81]
	v_mfma_f32_32x32x16_bf16 v[50:65], v[118:121], v[94:97], v[50:65]
	s_waitcnt lgkmcnt(0)
	v_mfma_f32_32x32x16_bf16 v[34:49], v[98:101], v[82:85], v[34:49]
	v_add_f32_e32 v210, v16, v210
	v_mfma_f32_32x32x16_bf16 v[18:33], v[182:185], v[82:85], v[18:33]
	v_mfma_f32_32x32x16_bf16 v[34:49], v[102:105], v[90:93], v[34:49]
	v_mfma_f32_32x32x16_bf16 v[18:33], v[186:189], v[90:93], v[18:33]
	v_mfma_f32_32x32x16_bf16 v[34:49], v[106:109], v[86:89], v[34:49]
	v_mfma_f32_32x32x16_bf16 v[18:33], v[190:193], v[86:89], v[18:33]
	v_mfma_f32_32x32x16_bf16 v[34:49], v[110:113], v[94:97], v[34:49]
	v_mfma_f32_32x32x16_bf16 v[18:33], v[222:225], v[94:97], v[18:33]

.LBB0_530:
	s_cmp_le_i32 s14, s19
	s_mov_b64 s[0:1], -1
	s_cbranch_scc0 .LBB0_536
	v_add3_u32 v2, s21, v217, v196
	ds_read_b128 v[4:7], v2
	ds_read_b128 v[8:11], v2 offset:32
	ds_read_b128 v[12:15], v2 offset:8704
	ds_read_b128 v[114:117], v2 offset:8736
	ds_read_b128 v[118:121], v2 offset:64
	ds_read_b128 v[122:125], v2 offset:96
	ds_read_b128 v[126:129], v2 offset:8768
	ds_read_b128 v[130:133], v2 offset:8800
	s_waitcnt lgkmcnt(7)
	v_mfma_f32_32x32x16_bf16 v[98:113], v[4:7], v[174:177], 0
	s_waitcnt lgkmcnt(5)
	v_mfma_f32_32x32x16_bf16 v[82:97], v[12:15], v[174:177], 0
	v_mfma_f32_32x32x16_bf16 v[98:113], v[8:11], v[170:173], v[98:113]
	s_waitcnt lgkmcnt(4)
	v_mfma_f32_32x32x16_bf16 v[82:97], v[114:117], v[170:173], v[82:97]
	s_waitcnt lgkmcnt(3)
	v_mfma_f32_32x32x16_bf16 v[98:113], v[118:121], v[166:169], v[98:113]
	s_waitcnt lgkmcnt(1)
	v_mfma_f32_32x32x16_bf16 v[82:97], v[126:129], v[166:169], v[82:97]
	v_mfma_f32_32x32x16_bf16 v[98:113], v[122:125], v[162:165], v[98:113]
	s_waitcnt lgkmcnt(0)
	v_mfma_f32_32x32x16_bf16 v[82:97], v[130:133], v[162:165], v[82:97]
	ds_read_b128 v[4:7], v2 offset:128
	ds_read_b128 v[8:11], v2 offset:160
	ds_read_b128 v[12:15], v2 offset:8832
	ds_read_b128 v[114:117], v2 offset:8864
	ds_read_b128 v[118:121], v2 offset:192
	ds_read_b128 v[122:125], v2 offset:224
	ds_read_b128 v[126:129], v2 offset:8896
	ds_read_b128 v[130:133], v2 offset:8928
	s_waitcnt lgkmcnt(7)
	v_mfma_f32_32x32x16_bf16 v[98:113], v[4:7], v[158:161], v[98:113]
	v_add_u32_e32 v2, s21, v199
	v_add_u32_e32 v2, v2, v197
	v_add_u32_e32 v4, 0x4000, v2
	s_waitcnt lgkmcnt(5)
	v_mfma_f32_32x32x16_bf16 v[82:97], v[12:15], v[158:161], v[82:97]
	ds_read2_b64 v[166:169], v4 offset0:128 offset1:130
	ds_read2_b64 v[158:161], v4 offset0:132 offset1:134
	v_mfma_f32_32x32x16_bf16 v[98:113], v[8:11], v[154:157], v[98:113]
	s_waitcnt lgkmcnt(6)
	v_mfma_f32_32x32x16_bf16 v[82:97], v[114:117], v[154:157], v[82:97]
	ds_read2_b64 v[162:165], v4 offset0:136 offset1:138
	ds_read2_b64 v[154:157], v4 offset0:140 offset1:142
	v_add_u32_e32 v4, 0x5000, v2
	s_waitcnt lgkmcnt(7)
	v_mfma_f32_32x32x16_bf16 v[98:113], v[118:121], v[150:153], v[98:113]
	s_waitcnt lgkmcnt(5)
	v_mfma_f32_32x32x16_bf16 v[82:97], v[126:129], v[150:153], v[82:97]
	ds_read2_b64 v[150:153], v4 offset0:160 offset1:162
	ds_read2_b64 v[12:15], v4 offset0:164 offset1:166
	ds_read2_b64 v[8:11], v4 offset0:168 offset1:170
	ds_read2_b64 v[4:7], v4 offset0:172 offset1:174
	v_mfma_f32_32x32x16_bf16 v[98:113], v[122:125], v[146:149], v[98:113]
	s_waitcnt lgkmcnt(8)
	v_mfma_f32_32x32x16_bf16 v[82:97], v[130:133], v[146:149], v[82:97]
	v_lshl_add_u32 v16, v1, 2, s21
	ds_read_b128 v[114:117], v16 offset:34816
	ds_read_b128 v[118:121], v16 offset:34848
	ds_read_b128 v[122:125], v16 offset:34944
	ds_read_b128 v[126:129], v16 offset:34976
	ds_read_b128 v[130:133], v16 offset:34880
	ds_read_b128 v[134:137], v16 offset:34912
	ds_read_b128 v[138:141], v16 offset:35008
	ds_read_b128 v[142:145], v16 offset:35040
	s_waitcnt lgkmcnt(7)
	v_xor_b32_e32 v117, 0x80000000, v117
	v_xor_b32_e32 v116, 0x80000000, v116
	s_waitcnt lgkmcnt(6)
	v_xor_b32_e32 v121, 0x80000000, v121
	v_xor_b32_e32 v120, 0x80000000, v120
	s_mov_b32 s10, 0x3e0293ee
	s_or_b32 s0, s14, 63
	s_waitcnt lgkmcnt(3)
	v_xor_b32_e32 v133, 0x80000000, v133
	v_xor_b32_e32 v132, 0x80000000, v132
	s_waitcnt lgkmcnt(2)
	v_xor_b32_e32 v17, 0x80000000, v137
	v_xor_b32_e32 v16, 0x80000000, v136
	v_fma_f32 v176, v102, s10, -v118
	v_fma_f32 v177, v103, s10, -v119
	v_fma_f32 v178, v104, s10, v120
	v_fma_f32 v179, v105, s10, v121
	v_fma_f32 v198, v100, s10, v116
	v_fma_f32 v199, v101, s10, v117
	v_fma_f32 v200, v98, s10, -v114
	v_fma_f32 v201, v99, s10, -v115
	v_xor_b32_e32 v99, 0x80000000, v125
	v_xor_b32_e32 v98, 0x80000000, v124
	v_xor_b32_e32 v101, 0x80000000, v129
	v_xor_b32_e32 v100, 0x80000000, v128
	s_waitcnt lgkmcnt(1)
	v_xor_b32_e32 v103, 0x80000000, v141
	v_xor_b32_e32 v102, 0x80000000, v140
	s_waitcnt lgkmcnt(0)
	v_xor_b32_e32 v105, 0x80000000, v145
	v_xor_b32_e32 v104, 0x80000000, v144
	v_fma_f32 v146, v110, s10, -v134
	v_fma_f32 v147, v111, s10, -v135
	v_fma_f32 v148, v106, s10, -v130
	v_fma_f32 v149, v107, s10, -v131
	v_fma_f32 v16, v112, s10, v16
	v_fma_f32 v17, v113, s10, v17
	v_fma_f32 v170, v108, s10, v132
	v_fma_f32 v171, v109, s10, v133
	v_fma_f32 v174, v94, s10, -v142
	v_fma_f32 v175, v95, s10, -v143
	v_fma_f32 v180, v90, s10, -v138
	v_fma_f32 v181, v91, s10, -v139
	v_fma_f32 v202, v86, s10, -v126
	v_fma_f32 v203, v87, s10, -v127
	v_fma_f32 v172, v96, s10, v104
	v_fma_f32 v173, v97, s10, v105
	v_fma_f32 v196, v92, s10, v102
	v_fma_f32 v197, v93, s10, v103
	v_fma_f32 v204, v88, s10, v100
	v_fma_f32 v205, v89, s10, v101
	v_fma_f32 v206, v84, s10, v98
	v_fma_f32 v207, v85, s10, v99
	s_cmp_le_i32 s0, s18
	v_fma_f32 v208, v82, s10, -v122
	v_fma_f32 v209, v83, s10, -v123
	s_cbranch_scc1 .LBB0_533
	v_or_b32_e32 v82, s14, v1
	v_or_b32_e32 v83, 32, v82
	v_cmp_le_i32_e32 vcc, v83, v211
	v_or_b32_e32 v83, 33, v82
	s_nop 0
	v_cndmask_b32_e32 v208, v229, v208, vcc
	v_cmp_lt_i32_e32 vcc, v82, v211
	s_nop 1
	v_cndmask_b32_e32 v201, v229, v201, vcc
	v_cmp_le_i32_e32 vcc, v82, v211
	s_nop 1
	v_cndmask_b32_e32 v200, v229, v200, vcc
	v_cmp_le_i32_e32 vcc, v83, v211
	v_or_b32_e32 v83, 2, v82
	s_nop 0
	v_cndmask_b32_e32 v209, v229, v209, vcc
	v_cmp_le_i32_e32 vcc, v83, v211
	v_or_b32_e32 v83, 34, v82
	s_nop 0
	v_cndmask_b32_e32 v198, v229, v198, vcc
	v_cmp_le_i32_e32 vcc, v83, v211
	v_or_b32_e32 v83, 3, v82
	s_nop 0
	v_cndmask_b32_e32 v206, v229, v206, vcc
	v_cmp_le_i32_e32 vcc, v83, v211
	v_or_b32_e32 v83, 35, v82
	s_nop 0
	v_cndmask_b32_e32 v199, v229, v199, vcc
	v_cmp_le_i32_e32 vcc, v83, v211
	v_or_b32_e32 v83, 8, v82
	s_nop 0
	v_cndmask_b32_e32 v207, v229, v207, vcc
	v_cmp_le_i32_e32 vcc, v83, v211
	v_or_b32_e32 v83, 40, v82
	s_nop 0
	v_cndmask_b32_e32 v176, v229, v176, vcc
	v_cmp_le_i32_e32 vcc, v83, v211
	v_or_b32_e32 v83, 9, v82
	s_nop 0
	v_cndmask_b32_e32 v202, v229, v202, vcc
	v_cmp_le_i32_e32 vcc, v83, v211
	v_or_b32_e32 v83, 41, v82
	s_nop 0
	v_cndmask_b32_e32 v177, v229, v177, vcc
	v_cmp_le_i32_e32 vcc, v83, v211
	v_or_b32_e32 v83, 10, v82
	s_nop 0
	v_cndmask_b32_e32 v203, v229, v203, vcc
	v_cmp_le_i32_e32 vcc, v83, v211
	v_or_b32_e32 v83, 42, v82
	s_nop 0
	v_cndmask_b32_e32 v178, v229, v178, vcc
	v_cmp_le_i32_e32 vcc, v83, v211
	v_or_b32_e32 v83, 11, v82
	s_nop 0
	v_cndmask_b32_e32 v204, v229, v204, vcc
	v_cmp_le_i32_e32 vcc, v83, v211
	v_or_b32_e32 v83, 43, v82
	s_nop 0
	v_cndmask_b32_e32 v179, v229, v179, vcc
	v_cmp_le_i32_e32 vcc, v83, v211
	v_or_b32_e32 v83, 16, v82
	s_nop 0
	v_cndmask_b32_e32 v205, v229, v205, vcc
	v_cmp_le_i32_e32 vcc, v83, v211
	v_or_b32_e32 v83, 48, v82
	s_nop 0
	v_cndmask_b32_e32 v148, v229, v148, vcc
	v_cmp_le_i32_e32 vcc, v83, v211
	v_or_b32_e32 v83, 17, v82
	s_nop 0
	v_cndmask_b32_e32 v180, v229, v180, vcc
	v_cmp_le_i32_e32 vcc, v83, v211
	v_or_b32_e32 v83, 49, v82
	s_nop 0
	v_cndmask_b32_e32 v149, v229, v149, vcc
	v_cmp_le_i32_e32 vcc, v83, v211
	v_or_b32_e32 v83, 18, v82
	s_nop 0
	v_cndmask_b32_e32 v181, v229, v181, vcc
	v_cmp_le_i32_e32 vcc, v83, v211
	v_or_b32_e32 v83, 50, v82
	s_nop 0
	v_cndmask_b32_e32 v170, v229, v170, vcc
	v_cmp_le_i32_e32 vcc, v83, v211
	v_or_b32_e32 v83, 19, v82
	s_nop 0
	v_cndmask_b32_e32 v196, v229, v196, vcc
	v_cmp_le_i32_e32 vcc, v83, v211
	v_or_b32_e32 v83, 51, v82
	s_nop 0
	v_cndmask_b32_e32 v171, v229, v171, vcc
	v_cmp_le_i32_e32 vcc, v83, v211
	v_or_b32_e32 v83, 24, v82
	s_nop 0
	v_cndmask_b32_e32 v197, v229, v197, vcc
	v_cmp_le_i32_e32 vcc, v83, v211
	v_or_b32_e32 v83, 56, v82
	s_nop 0
	v_cndmask_b32_e32 v146, v229, v146, vcc
	v_cmp_le_i32_e32 vcc, v83, v211
	v_or_b32_e32 v83, 25, v82
	s_nop 0
	v_cndmask_b32_e32 v174, v229, v174, vcc
	v_cmp_le_i32_e32 vcc, v83, v211
	v_or_b32_e32 v83, 57, v82
	s_nop 0
	v_cndmask_b32_e32 v147, v229, v147, vcc
	v_cmp_le_i32_e32 vcc, v83, v211
	v_or_b32_e32 v83, 26, v82
	s_nop 0
	v_cndmask_b32_e32 v175, v229, v175, vcc
	v_cmp_le_i32_e32 vcc, v83, v211
	v_or_b32_e32 v83, 58, v82
	s_nop 0
	v_cndmask_b32_e32 v16, v229, v16, vcc
	v_cmp_le_i32_e32 vcc, v83, v211
	v_or_b32_e32 v83, 27, v82
	v_or_b32_e32 v82, 59, v82
	v_cndmask_b32_e32 v172, v229, v172, vcc
	v_cmp_le_i32_e32 vcc, v83, v211
	s_nop 1
	v_cndmask_b32_e32 v17, v229, v17, vcc
	v_cmp_le_i32_e32 vcc, v82, v211
	s_nop 1
	v_cndmask_b32_e32 v173, v229, v173, vcc
.LBB0_533:
	v_max3_f32 v82, v229, v200, v208
	v_max3_f32 v83, v229, v201, v209
	v_mbcnt_hi_u32_b32 v214, -1, v251
	v_max3_f32 v82, v82, v198, v206
	v_max3_f32 v83, v83, v199, v207
	v_xor_b32_e32 v213, 32, v214
	v_max3_f32 v82, v82, v176, v202
	v_max3_f32 v83, v83, v177, v203
	v_mov_b64_e32 v[112:113], v[48:49]
	v_max3_f32 v82, v82, v178, v204
	v_max3_f32 v83, v83, v179, v205
	v_mov_b64_e32 v[128:129], v[64:65]
	v_max3_f32 v82, v82, v148, v180
	v_max3_f32 v83, v83, v149, v181
	v_mov_b64_e32 v[144:145], v[80:81]
	v_max3_f32 v82, v82, v170, v196
	v_max3_f32 v83, v83, v171, v197
	v_mov_b64_e32 v[110:111], v[46:47]
	v_max3_f32 v82, v82, v146, v174
	v_max3_f32 v83, v83, v147, v175
	v_mov_b64_e32 v[108:109], v[44:45]
	v_max3_f32 v82, v82, v16, v172
	v_max3_f32 v83, v83, v17, v173
	v_mov_b64_e32 v[106:107], v[42:43]
	v_max_f32 v82, v82, v83
	v_and_b32_e32 v83, 64, v214
	v_add_u32_e32 v215, 64, v83
	v_cmp_lt_i32_e32 vcc, v213, v215
	v_mov_b64_e32 v[104:105], v[40:41]
	v_mov_b64_e32 v[102:103], v[38:39]
	v_cndmask_b32_e32 v83, v214, v213, vcc
	v_lshlrev_b32_e32 v83, 2, v83
	ds_bpermute_b32 v83, v83, v82
	v_mov_b64_e32 v[100:101], v[36:37]
	v_mov_b64_e32 v[98:99], v[34:35]
	v_mov_b64_e32 v[126:127], v[62:63]
	v_mov_b64_e32 v[124:125], v[60:61]
	s_waitcnt lgkmcnt(0)
	v_max3_f32 v211, v212, v82, v83
	v_mov_b64_e32 v[96:97], v[32:33]
	v_cmp_gt_f32_e32 vcc, v211, v212
	v_mov_b64_e32 v[94:95], v[30:31]
	v_mov_b64_e32 v[92:93], v[28:29]
	v_mov_b64_e32 v[90:91], v[26:27]
	v_mov_b64_e32 v[88:89], v[24:25]
	v_mov_b64_e32 v[86:87], v[22:23]
	v_mov_b64_e32 v[84:85], v[20:21]
	v_mov_b64_e32 v[82:83], v[18:19]
	v_mov_b64_e32 v[122:123], v[58:59]
	v_mov_b64_e32 v[120:121], v[56:57]
	v_mov_b64_e32 v[118:119], v[54:55]
	v_mov_b64_e32 v[116:117], v[52:53]
	v_mov_b64_e32 v[114:115], v[50:51]
	v_mov_b64_e32 v[142:143], v[78:79]
	v_mov_b64_e32 v[140:141], v[76:77]
	v_mov_b64_e32 v[138:139], v[74:75]
	v_mov_b64_e32 v[136:137], v[72:73]
	v_mov_b64_e32 v[134:135], v[70:71]
	v_mov_b64_e32 v[132:133], v[68:69]
	v_mov_b64_e32 v[130:131], v[66:67]
	v_mov_b32_e32 v216, v210
	s_cbranch_vccz .LBB0_535
	v_sub_f32_e32 v82, v212, v211
	v_exp_f32_e32 v182, v82
	s_nop 0
	v_mul_f32_e32 v144, v80, v182
	v_mul_f32_e32 v145, v81, v182
	v_mul_f32_e32 v142, v78, v182
	v_mul_f32_e32 v143, v79, v182
	v_mul_f32_e32 v140, v76, v182
	v_mul_f32_e32 v141, v77, v182
	v_mul_f32_e32 v138, v74, v182
	v_mul_f32_e32 v139, v75, v182
	v_mul_f32_e32 v136, v72, v182
	v_mul_f32_e32 v137, v73, v182
	v_mul_f32_e32 v134, v70, v182
	v_mul_f32_e32 v135, v71, v182
	v_mul_f32_e32 v132, v68, v182
	v_mul_f32_e32 v133, v69, v182
	v_mul_f32_e32 v130, v66, v182
	v_mul_f32_e32 v131, v67, v182
	v_mul_f32_e32 v128, v64, v182
	v_mul_f32_e32 v129, v65, v182
	v_mul_f32_e32 v126, v62, v182
	v_mul_f32_e32 v127, v63, v182
	v_mul_f32_e32 v124, v60, v182
	v_mul_f32_e32 v125, v61, v182
	v_mul_f32_e32 v122, v58, v182
	v_mul_f32_e32 v123, v59, v182
	v_mul_f32_e32 v120, v56, v182
	v_mul_f32_e32 v121, v57, v182
	v_mul_f32_e32 v118, v54, v182
	v_mul_f32_e32 v119, v55, v182
	v_mul_f32_e32 v116, v52, v182
	v_mul_f32_e32 v117, v53, v182
	v_mul_f32_e32 v114, v50, v182
	v_mul_f32_e32 v115, v51, v182
	v_mul_f32_e32 v112, v48, v182
	v_mul_f32_e32 v113, v49, v182
	v_mul_f32_e32 v110, v46, v182
	v_mul_f32_e32 v111, v47, v182
	v_mul_f32_e32 v108, v44, v182
	v_mul_f32_e32 v109, v45, v182
	v_mul_f32_e32 v106, v42, v182
	v_mul_f32_e32 v107, v43, v182
	v_mul_f32_e32 v104, v40, v182
	v_mul_f32_e32 v105, v41, v182
	v_mul_f32_e32 v102, v38, v182
	v_mul_f32_e32 v103, v39, v182
	v_mul_f32_e32 v100, v36, v182
	v_mul_f32_e32 v101, v37, v182
	v_mul_f32_e32 v98, v34, v182
	v_mul_f32_e32 v99, v35, v182
	v_mul_f32_e32 v96, v32, v182
	v_mul_f32_e32 v97, v33, v182
	v_mul_f32_e32 v94, v30, v182
	v_mul_f32_e32 v95, v31, v182
	v_mul_f32_e32 v92, v28, v182
	v_mul_f32_e32 v93, v29, v182
	v_mul_f32_e32 v90, v26, v182
	v_mul_f32_e32 v91, v27, v182
	v_mul_f32_e32 v88, v24, v182
	v_mul_f32_e32 v89, v25, v182
	v_mul_f32_e32 v86, v22, v182
	v_mul_f32_e32 v87, v23, v182
	v_mul_f32_e32 v84, v20, v182
	v_mul_f32_e32 v85, v21, v182
	v_mul_f32_e32 v82, v18, v182
	v_mul_f32_e32 v83, v19, v182
	v_mul_f32_e32 v216, v210, v182
.LBB0_535:
	v_sub_f32_e32 v182, v200, v211
	v_exp_f32_e32 v212, v182
	v_sub_f32_e32 v182, v208, v211
	v_exp_f32_e32 v217, v182
	v_sub_f32_e32 v182, v201, v211
	v_exp_f32_e32 v220, v182
	v_sub_f32_e32 v182, v209, v211
	v_exp_f32_e32 v221, v182
	v_sub_f32_e32 v182, v198, v211
	v_exp_f32_e32 v224, v182
	v_sub_f32_e32 v182, v206, v211
	v_sub_f32_e32 v176, v176, v211
	v_exp_f32_e32 v225, v182
	v_sub_f32_e32 v182, v199, v211
	v_exp_f32_e32 v183, v176
	v_sub_f32_e32 v176, v202, v211
	v_exp_f32_e32 v232, v182
	v_sub_f32_e32 v182, v207, v211
	v_exp_f32_e32 v185, v176
	v_sub_f32_e32 v176, v177, v211
	v_exp_f32_e32 v233, v182
	v_exp_f32_e32 v182, v176
	v_sub_f32_e32 v176, v203, v211
	v_exp_f32_e32 v184, v176
	v_sub_f32_e32 v176, v178, v211
	v_exp_f32_e32 v177, v176
	v_sub_f32_e32 v176, v204, v211
	v_sub_f32_e32 v148, v148, v211
	v_exp_f32_e32 v187, v176
	v_sub_f32_e32 v176, v179, v211
	v_exp_f32_e32 v179, v148
	v_sub_f32_e32 v148, v180, v211
	v_sub_f32_e32 v178, v205, v211
	v_exp_f32_e32 v193, v148
	v_sub_f32_e32 v148, v149, v211
	v_exp_f32_e32 v186, v178
	v_exp_f32_e32 v178, v148
	v_sub_f32_e32 v148, v181, v211
	v_exp_f32_e32 v192, v148
	v_sub_f32_e32 v148, v170, v211
	v_exp_f32_e32 v181, v148
	v_sub_f32_e32 v148, v196, v211
	v_exp_f32_e32 v199, v148
	v_sub_f32_e32 v148, v171, v211
	v_sub_f32_e32 v146, v146, v211
	v_sub_f32_e32 v16, v16, v211
	v_exp_f32_e32 v180, v148
	v_sub_f32_e32 v148, v197, v211
	v_exp_f32_e32 v197, v146
	v_sub_f32_e32 v146, v174, v211
	v_exp_f32_e32 v203, v16
	v_sub_f32_e32 v16, v172, v211
	v_exp_f32_e32 v176, v176
	v_exp_f32_e32 v201, v146
	v_sub_f32_e32 v146, v147, v211
	v_exp_f32_e32 v205, v16
	v_sub_f32_e32 v16, v17, v211
	v_exp_f32_e32 v196, v146
	v_exp_f32_e32 v202, v16
	v_exp_f32_e32 v198, v148
	v_sub_f32_e32 v146, v175, v211
	v_sub_f32_e32 v16, v173, v211
	v_exp_f32_e32 v200, v146
	v_exp_f32_e32 v204, v16
	v_pk_mov_b32 v[172:173], v[184:185], v[184:185] op_sel:[1,0]
	v_pk_mov_b32 v[174:175], v[186:187], v[186:187] op_sel:[1,0]
	v_add_f32_e32 v190, v176, v186
	v_add_f32_e32 v191, v177, v187
	v_pk_mov_b32 v[170:171], v[176:177], v[176:177] op_sel:[1,0]
	v_cvt_pk_bf16_f32 v172, v172, v173
	v_cvt_pk_bf16_f32 v173, v174, v175
	v_pk_mov_b32 v[174:175], v[178:179], v[178:179] op_sel:[1,0]
	v_pk_mov_b32 v[176:177], v[180:181], v[180:181] op_sel:[1,0]
	v_add_f32_e32 v16, v178, v192
	v_add_f32_e32 v17, v179, v193
	v_cvt_pk_bf16_f32 v174, v174, v175
	v_cvt_pk_bf16_f32 v175, v176, v177
	v_pk_mov_b32 v[176:177], v[196:197], v[196:197] op_sel:[1,0]
	v_pk_mov_b32 v[178:179], v[202:203], v[202:203] op_sel:[1,0]
	v_add_f32_e32 v206, v180, v198
	v_add_f32_e32 v207, v181, v199
	v_cvt_pk_bf16_f32 v176, v176, v177
	v_cvt_pk_bf16_f32 v177, v178, v179
	v_pk_mov_b32 v[178:179], v[192:193], v[192:193] op_sel:[1,0]
	v_pk_mov_b32 v[180:181], v[198:199], v[198:199] op_sel:[1,0]
	v_add_f32_e32 v222, v212, v217
	v_add_f32_e32 v188, v182, v184
	v_add_f32_e32 v189, v183, v185
	v_pk_mov_b32 v[148:149], v[182:183], v[182:183] op_sel:[1,0]
	v_cvt_pk_bf16_f32 v178, v178, v179
	v_cvt_pk_bf16_f32 v179, v180, v181
	v_pk_mov_b32 v[180:181], v[200:201], v[200:201] op_sel:[1,0]
	v_pk_mov_b32 v[182:183], v[204:205], v[204:205] op_sel:[1,0]
	v_add_f32_e32 v223, v220, v221
	v_cvt_pk_bf16_f32 v180, v180, v181
	v_cvt_pk_bf16_f32 v181, v182, v183
	v_add_f32_e32 v182, 0, v222
	v_add_f32_e32 v234, v224, v225
	v_add_f32_e32 v182, v223, v182
	v_add_f32_e32 v235, v232, v233
	v_add_f32_e32 v182, v234, v182
	v_add_f32_e32 v182, v235, v182
	v_add_f32_e32 v182, v189, v182
	v_add_f32_e32 v182, v188, v182
	v_add_f32_e32 v182, v191, v182
	v_add_f32_e32 v182, v190, v182
	v_add_f32_e32 v17, v17, v182
	v_add_f32_e32 v16, v16, v17
	v_add_f32_e32 v16, v207, v16
	v_add_f32_e32 v208, v196, v200
	v_add_f32_e32 v209, v197, v201
	v_add_f32_e32 v16, v206, v16
	v_add_f32_e32 v16, v209, v16
	v_add_f32_e32 v218, v202, v204
	v_add_f32_e32 v219, v203, v205
	v_add_f32_e32 v16, v208, v16
	v_add_f32_e32 v16, v219, v16
	v_cvt_pk_bf16_f32 v146, v212, v220
	v_cvt_pk_bf16_f32 v147, v224, v232
	v_cvt_pk_bf16_f32 v148, v148, v149
	v_cvt_pk_bf16_f32 v149, v170, v171
	v_cvt_pk_bf16_f32 v170, v217, v221
	v_cvt_pk_bf16_f32 v171, v225, v233
	v_add_f32_e32 v16, v218, v16
	v_add_u32_e32 v17, 0x6000, v2
	v_add_u32_e32 v2, 0x7000, v2
	ds_read2_b64 v[182:185], v17 offset0:192 offset1:194
	ds_read2_b64 v[186:189], v17 offset0:196 offset1:198
	ds_read2_b64 v[196:199], v17 offset0:200 offset1:202
	ds_read2_b64 v[200:203], v17 offset0:204 offset1:206
	ds_read2_b64 v[204:207], v2 offset0:224 offset1:226
	ds_read2_b64 v[218:221], v2 offset0:228 offset1:230
	ds_read2_b64 v[222:225], v2 offset0:232 offset1:234
	ds_read2_b64 v[232:235], v2 offset0:236 offset1:238
	v_mfma_f32_32x32x16_bf16 v[130:145], v[166:169], v[146:149], v[130:145]
	v_mfma_f32_32x32x16_bf16 v[114:129], v[150:153], v[146:149], v[114:129]
	v_mfma_f32_32x32x16_bf16 v[130:145], v[158:161], v[174:177], v[130:145]
	v_mfma_f32_32x32x16_bf16 v[114:129], v[12:15], v[174:177], v[114:129]
	v_mfma_f32_32x32x16_bf16 v[130:145], v[162:165], v[170:173], v[130:145]
	v_mfma_f32_32x32x16_bf16 v[114:129], v[8:11], v[170:173], v[114:129]
	v_mfma_f32_32x32x16_bf16 v[130:145], v[154:157], v[178:181], v[130:145]
	v_mfma_f32_32x32x16_bf16 v[114:129], v[4:7], v[178:181], v[114:129]
	s_waitcnt lgkmcnt(7)
	v_mfma_f32_32x32x16_bf16 v[98:113], v[182:185], v[146:149], v[98:113]
	v_add_f32_e32 v2, v16, v216
	s_mov_b64 s[0:1], 0
	s_waitcnt lgkmcnt(3)
	v_mfma_f32_32x32x16_bf16 v[82:97], v[204:207], v[146:149], v[82:97]
	v_mfma_f32_32x32x16_bf16 v[98:113], v[186:189], v[174:177], v[98:113]
	s_waitcnt lgkmcnt(2)
	v_mfma_f32_32x32x16_bf16 v[82:97], v[218:221], v[174:177], v[82:97]
	v_mfma_f32_32x32x16_bf16 v[98:113], v[196:199], v[170:173], v[98:113]
	s_waitcnt lgkmcnt(1)
	v_mfma_f32_32x32x16_bf16 v[82:97], v[222:225], v[170:173], v[82:97]
	v_mfma_f32_32x32x16_bf16 v[98:113], v[200:203], v[178:181], v[98:113]
	s_waitcnt lgkmcnt(0)
	v_mfma_f32_32x32x16_bf16 v[82:97], v[232:235], v[178:181], v[82:97]

.LBB0_1144:
	s_cmp_gt_i32 s19, s5
	s_cselect_b64 s[22:23], -1, 0
	s_cmp_lt_i32 s19, s18
	s_cselect_b64 s[24:25], -1, 0
	s_or_b64 s[22:23], s[22:23], s[24:25]
	s_and_b64 vcc, exec, s[22:23]
	s_cbranch_vccnz .LBB0_1148
	s_bitcmp1_b32 s21, 0
	s_cselect_b32 s21, 0x8900, 0
	s_add_i32 s21, s72, s21
	v_add3_u32 v176, s21, v1, v2
	ds_read_b128 v[68:71], v176
	ds_read_b128 v[148:151], v176 offset:32
	ds_read_b128 v[72:75], v176 offset:8704
	ds_read_b128 v[152:155], v176 offset:8736
	ds_read_b128 v[156:159], v176 offset:64
	ds_read_b128 v[160:163], v176 offset:96
	ds_read_b128 v[164:167], v176 offset:8768
	ds_read_b128 v[168:171], v176 offset:8800
	s_waitcnt lgkmcnt(0)
	v_mfma_f32_32x32x16_bf16 v[84:99], v[68:71], v[128:131], 0
	v_mfma_f32_32x32x16_bf16 v[68:83], v[72:75], v[128:131], 0
	v_mfma_f32_32x32x16_bf16 v[84:99], v[148:151], v[124:127], v[84:99]
	v_mfma_f32_32x32x16_bf16 v[68:83], v[152:155], v[124:127], v[68:83]
	v_mfma_f32_32x32x16_bf16 v[84:99], v[156:159], v[120:123], v[84:99]
	v_mfma_f32_32x32x16_bf16 v[68:83], v[164:167], v[120:123], v[68:83]
	v_mfma_f32_32x32x16_bf16 v[84:99], v[160:163], v[116:119], v[84:99]
	v_mfma_f32_32x32x16_bf16 v[68:83], v[168:171], v[116:119], v[68:83]
	ds_read_b128 v[148:151], v176 offset:128
	ds_read_b128 v[152:155], v176 offset:160
	ds_read_b128 v[156:159], v176 offset:8832
	ds_read_b128 v[160:163], v176 offset:8864
	ds_read_b128 v[164:167], v176 offset:192
	ds_read_b128 v[172:175], v176 offset:224
	ds_read_b128 v[168:171], v176 offset:8896
	ds_read_b128 v[182:185], v176 offset:8928
	s_waitcnt lgkmcnt(0)
	v_mfma_f32_32x32x16_bf16 v[84:99], v[148:151], v[112:115], v[84:99]
	v_add_u32_e32 v148, s21, v212
	v_add_u32_e32 v197, v148, v211
	v_add_u32_e32 v148, 0x4000, v197
	v_mfma_f32_32x32x16_bf16 v[68:83], v[156:159], v[112:115], v[68:83]
	v_mfma_f32_32x32x16_bf16 v[84:99], v[152:155], v[108:111], v[84:99]
	v_mfma_f32_32x32x16_bf16 v[68:83], v[160:163], v[108:111], v[68:83]
	v_mfma_f32_32x32x16_bf16 v[84:99], v[164:167], v[104:107], v[84:99]
	v_mfma_f32_32x32x16_bf16 v[68:83], v[168:171], v[104:107], v[68:83]
	ds_read2_b64 v[176:179], v148 offset0:128 offset1:130
	ds_read2_b64 v[168:171], v148 offset0:132 offset1:134
	v_mfma_f32_32x32x16_bf16 v[84:99], v[172:175], v[100:103], v[84:99]
	ds_read2_b64 v[172:175], v148 offset0:136 offset1:138
	ds_read2_b64 v[164:167], v148 offset0:140 offset1:142
	v_add_u32_e32 v148, 0x5000, v197
	ds_read2_b64 v[160:163], v148 offset0:160 offset1:162
	ds_read2_b64 v[156:159], v148 offset0:164 offset1:166
	ds_read2_b64 v[152:155], v148 offset0:168 offset1:170
	ds_read2_b64 v[148:151], v148 offset0:172 offset1:174
	v_mfma_f32_32x32x16_bf16 v[68:83], v[182:185], v[100:103], v[68:83]
	v_cvt_f32_i32_e32 v182, v195
	s_add_i32 s21, s19, 63
	s_cmp_le_i32 s21, s16
	v_mul_f32_e32 v182, v208, v182
	v_exp_f32_e32 v204, v182
	ds_read_b128 v[182:185], v213
	ds_read_b128 v[186:189], v213 offset:32
	ds_read_b128 v[190:193], v214
	ds_read_b128 v[222:225], v214 offset:32
	ds_read_b128 v[232:235], v213 offset:64
	ds_read_b128 v[236:239], v213 offset:96
	ds_read_b128 v[242:245], v214 offset:64
	ds_read_b128 v[246:249], v214 offset:96
	v_mul_f32_e32 v250, 0x3db504f3, v204
	s_waitcnt lgkmcnt(0)
	v_mul_f32_e32 v184, v250, v184
	v_mul_f32_e32 v185, v250, v185
	v_mul_f32_e32 v188, v250, v188
	v_mul_f32_e32 v189, v250, v189
	v_mul_f32_e32 v238, v250, v238
	v_mul_f32_e32 v239, v250, v239
	v_mul_f32_e32 v182, v250, v182
	v_mul_f32_e32 v183, v250, v183
	v_mul_f32_e32 v186, v250, v186
	v_mul_f32_e32 v187, v250, v187
	v_mul_f32_e32 v204, v250, v232
	v_mul_f32_e32 v205, v250, v233
	v_mul_f32_e32 v234, v250, v234
	v_mul_f32_e32 v235, v250, v235
	v_mul_f32_e32 v232, v250, v236
	v_mul_f32_e32 v233, v250, v237
	v_mul_f32_e32 v92, v92, v204
	v_mul_f32_e32 v93, v93, v205
	v_mul_f32_e32 v204, v88, v186
	v_mul_f32_e32 v205, v89, v187
	v_mul_f32_e32 v88, v98, v238
	v_mul_f32_e32 v89, v99, v239
	v_mul_f32_e32 v90, v90, v188
	v_mul_f32_e32 v91, v91, v189
	v_mul_f32_e32 v86, v86, v184
	v_mul_f32_e32 v87, v87, v185
	v_mul_f32_e32 v84, v84, v182
	v_mul_f32_e32 v85, v85, v183
	v_mul_f32_e32 v182, v250, v192
	v_mul_f32_e32 v183, v250, v193
	v_mul_f32_e32 v184, v250, v224
	v_mul_f32_e32 v185, v250, v225
	v_mul_f32_e32 v186, v250, v244
	v_mul_f32_e32 v187, v250, v245
	v_mul_f32_e32 v188, v250, v248
	v_mul_f32_e32 v189, v250, v249
	v_mul_f32_e32 v190, v250, v190
	v_mul_f32_e32 v191, v250, v191
	v_mul_f32_e32 v98, v250, v222
	v_mul_f32_e32 v99, v250, v223
	v_mul_f32_e32 v192, v250, v242
	v_mul_f32_e32 v193, v250, v243
	v_mul_f32_e32 v222, v250, v246
	v_mul_f32_e32 v223, v250, v247
	v_mul_f32_e32 v96, v96, v232
	v_mul_f32_e32 v97, v97, v233
	v_mul_f32_e32 v94, v94, v234
	v_mul_f32_e32 v95, v95, v235
	v_mul_f32_e32 v80, v80, v222
	v_mul_f32_e32 v81, v81, v223
	v_mul_f32_e32 v76, v76, v192
	v_mul_f32_e32 v77, v77, v193
	v_mul_f32_e32 v98, v72, v98
	v_mul_f32_e32 v99, v73, v99
	v_mul_f32_e32 v72, v82, v188
	v_mul_f32_e32 v73, v83, v189
	v_mul_f32_e32 v78, v78, v186
	v_mul_f32_e32 v79, v79, v187
	v_mul_f32_e32 v74, v74, v184
	v_mul_f32_e32 v75, v75, v185
	v_mul_f32_e32 v70, v70, v182
	v_mul_f32_e32 v71, v71, v183
	v_mul_f32_e32 v68, v68, v190
	v_mul_f32_e32 v69, v69, v191
	s_cbranch_scc1 .LBB0_1147
	v_add_u32_e32 v82, s19, v206
	v_add_u32_e32 v83, 32, v82
	v_cmp_le_i32_e32 vcc, v83, v207
	v_add_u32_e32 v83, 33, v82
	s_nop 0
	v_cndmask_b32_e32 v68, 0, v68, vcc
	v_cmp_lt_i32_e32 vcc, v82, v207
	s_nop 1
	v_cndmask_b32_e32 v85, 0, v85, vcc
	v_cmp_le_i32_e32 vcc, v82, v207
	s_nop 1
	v_cndmask_b32_e32 v84, 0, v84, vcc
	v_cmp_le_i32_e32 vcc, v83, v207
	v_add_u32_e32 v83, 2, v82
	s_nop 0
	v_cndmask_b32_e32 v69, 0, v69, vcc
	v_cmp_le_i32_e32 vcc, v83, v207
	v_add_u32_e32 v83, 34, v82
	s_nop 0
	v_cndmask_b32_e32 v86, 0, v86, vcc
	v_cmp_le_i32_e32 vcc, v83, v207
	v_add_u32_e32 v83, 3, v82
	s_nop 0
	v_cndmask_b32_e32 v70, 0, v70, vcc
	v_cmp_le_i32_e32 vcc, v83, v207
	v_add_u32_e32 v83, 35, v82
	s_nop 0
	v_cndmask_b32_e32 v87, 0, v87, vcc
	v_cmp_le_i32_e32 vcc, v83, v207
	v_add_u32_e32 v83, 8, v82
	s_nop 0
	v_cndmask_b32_e32 v71, 0, v71, vcc
	v_cmp_le_i32_e32 vcc, v83, v207
	v_add_u32_e32 v83, 40, v82
	s_nop 0
	v_cndmask_b32_e32 v204, 0, v204, vcc
	v_cmp_le_i32_e32 vcc, v83, v207
	v_add_u32_e32 v83, 9, v82
	s_nop 0
	v_cndmask_b32_e32 v98, 0, v98, vcc
	v_cmp_le_i32_e32 vcc, v83, v207
	v_add_u32_e32 v83, 41, v82
	s_nop 0
	v_cndmask_b32_e32 v205, 0, v205, vcc
	v_cmp_le_i32_e32 vcc, v83, v207
	v_add_u32_e32 v83, 10, v82
	s_nop 0
	v_cndmask_b32_e32 v99, 0, v99, vcc
	v_cmp_le_i32_e32 vcc, v83, v207
	v_add_u32_e32 v83, 42, v82
	s_nop 0
	v_cndmask_b32_e32 v90, 0, v90, vcc
	v_cmp_le_i32_e32 vcc, v83, v207
	v_add_u32_e32 v83, 11, v82
	s_nop 0
	v_cndmask_b32_e32 v74, 0, v74, vcc
	v_cmp_le_i32_e32 vcc, v83, v207
	v_add_u32_e32 v83, 43, v82
	s_nop 0
	v_cndmask_b32_e32 v91, 0, v91, vcc
	v_cmp_le_i32_e32 vcc, v83, v207
	v_add_u32_e32 v83, 16, v82
	s_nop 0
	v_cndmask_b32_e32 v75, 0, v75, vcc
	v_cmp_le_i32_e32 vcc, v83, v207
	v_add_u32_e32 v83, 48, v82
	s_nop 0
	v_cndmask_b32_e32 v92, 0, v92, vcc
	v_cmp_le_i32_e32 vcc, v83, v207
	v_add_u32_e32 v83, 17, v82
	s_nop 0
	v_cndmask_b32_e32 v76, 0, v76, vcc
	v_cmp_le_i32_e32 vcc, v83, v207
	v_add_u32_e32 v83, 49, v82
	s_nop 0
	v_cndmask_b32_e32 v93, 0, v93, vcc
	v_cmp_le_i32_e32 vcc, v83, v207
	v_add_u32_e32 v83, 18, v82
	s_nop 0
	v_cndmask_b32_e32 v77, 0, v77, vcc
	v_cmp_le_i32_e32 vcc, v83, v207
	v_add_u32_e32 v83, 50, v82
	s_nop 0
	v_cndmask_b32_e32 v94, 0, v94, vcc
	v_cmp_le_i32_e32 vcc, v83, v207
	v_add_u32_e32 v83, 19, v82
	s_nop 0
	v_cndmask_b32_e32 v78, 0, v78, vcc
	v_cmp_le_i32_e32 vcc, v83, v207
	v_add_u32_e32 v83, 51, v82
	s_nop 0
	v_cndmask_b32_e32 v95, 0, v95, vcc
	v_cmp_le_i32_e32 vcc, v83, v207
	v_add_u32_e32 v83, 24, v82
	s_nop 0
	v_cndmask_b32_e32 v79, 0, v79, vcc
	v_cmp_le_i32_e32 vcc, v83, v207
	v_add_u32_e32 v83, 56, v82
	s_nop 0
	v_cndmask_b32_e32 v96, 0, v96, vcc
	v_cmp_le_i32_e32 vcc, v83, v207
	v_add_u32_e32 v83, 25, v82
	s_nop 0
	v_cndmask_b32_e32 v80, 0, v80, vcc
	v_cmp_le_i32_e32 vcc, v83, v207
	v_add_u32_e32 v83, 57, v82
	s_nop 0
	v_cndmask_b32_e32 v97, 0, v97, vcc
	v_cmp_le_i32_e32 vcc, v83, v207
	v_add_u32_e32 v83, 26, v82
	s_nop 0
	v_cndmask_b32_e32 v81, 0, v81, vcc
	v_cmp_le_i32_e32 vcc, v83, v207
	v_add_u32_e32 v83, 58, v82
	s_nop 0
	v_cndmask_b32_e32 v88, 0, v88, vcc
	v_cmp_le_i32_e32 vcc, v83, v207
	v_add_u32_e32 v83, 27, v82
	v_add_u32_e32 v82, 59, v82
	v_cndmask_b32_e32 v72, 0, v72, vcc
	v_cmp_le_i32_e32 vcc, v83, v207
	s_nop 1
	v_cndmask_b32_e32 v89, 0, v89, vcc
	v_cmp_le_i32_e32 vcc, v82, v207
	s_nop 1
	v_cndmask_b32_e32 v73, 0, v73, vcc

.LBB0_1322:
	v_xor_b32_e32 v183, 32, v230
	v_cmp_lt_i32_e32 vcc, v183, v231
	s_waitcnt lgkmcnt(0)
	v_fmac_f32_e32 v205, v99, v153
	v_fmac_f32_e32 v203, v83, v153
	v_cndmask_b32_e32 v183, v230, v183, vcc
	v_bfe_i32 v83, v158, v198, 1
	v_bfe_i32 v182, v159, v198, 1
	v_lshlrev_b32_e32 v183, 2, v183
	v_bitop3_b32 v99, v205, s73, v83 bitop3:0xe4
	v_bitop3_b32 v83, v203, s73, v182 bitop3:0xe4
	v_max3_f32 v182, v204, v99, v83
	ds_bpermute_b32 v183, v183, v182
	s_waitcnt lgkmcnt(0)
	v_max3_f32 v203, v202, v182, v183
	v_cmp_gt_f32_e32 vcc, v203, v202
	s_cbranch_vccz .LBB0_1324
	v_sub_f32_e32 v182, v202, v203
	v_exp_f32_e32 v182, v182
	v_mov_b32_e32 v202, v203
	v_mul_f32_e32 v66, v66, v182
	v_mul_f32_e32 v67, v67, v182
	v_mul_f32_e32 v64, v64, v182
	v_mul_f32_e32 v65, v65, v182
	v_mul_f32_e32 v62, v62, v182
	v_mul_f32_e32 v63, v63, v182
	v_mul_f32_e32 v60, v60, v182
	v_mul_f32_e32 v61, v61, v182
	v_mul_f32_e32 v58, v58, v182
	v_mul_f32_e32 v59, v59, v182
	v_mul_f32_e32 v56, v56, v182
	v_mul_f32_e32 v57, v57, v182
	v_mul_f32_e32 v54, v54, v182
	v_mul_f32_e32 v55, v55, v182
	v_mul_f32_e32 v52, v52, v182
	v_mul_f32_e32 v53, v53, v182
	v_mul_f32_e32 v50, v50, v182
	v_mul_f32_e32 v51, v51, v182
	v_mul_f32_e32 v48, v48, v182
	v_mul_f32_e32 v49, v49, v182
	v_mul_f32_e32 v46, v46, v182
	v_mul_f32_e32 v47, v47, v182
	v_mul_f32_e32 v44, v44, v182
	v_mul_f32_e32 v45, v45, v182
	v_mul_f32_e32 v42, v42, v182
	v_mul_f32_e32 v43, v43, v182
	v_mul_f32_e32 v40, v40, v182
	v_mul_f32_e32 v41, v41, v182
	v_mul_f32_e32 v38, v38, v182
	v_mul_f32_e32 v39, v39, v182
	v_mul_f32_e32 v36, v36, v182
	v_mul_f32_e32 v37, v37, v182
	v_mul_f32_e32 v34, v34, v182
	v_mul_f32_e32 v35, v35, v182
	v_mul_f32_e32 v32, v32, v182
	v_mul_f32_e32 v33, v33, v182
	v_mul_f32_e32 v30, v30, v182
	v_mul_f32_e32 v31, v31, v182
	v_mul_f32_e32 v28, v28, v182
	v_mul_f32_e32 v29, v29, v182
	v_mul_f32_e32 v26, v26, v182
	v_mul_f32_e32 v27, v27, v182
	v_mul_f32_e32 v24, v24, v182
	v_mul_f32_e32 v25, v25, v182
	v_mul_f32_e32 v22, v22, v182
	v_mul_f32_e32 v23, v23, v182
	v_mul_f32_e32 v20, v20, v182
	v_mul_f32_e32 v21, v21, v182
	v_mul_f32_e32 v18, v18, v182
	v_mul_f32_e32 v19, v19, v182
	v_mul_f32_e32 v16, v16, v182
	v_mul_f32_e32 v17, v17, v182
	v_mul_f32_e32 v14, v14, v182
	v_mul_f32_e32 v15, v15, v182
	v_mul_f32_e32 v12, v12, v182
	v_mul_f32_e32 v13, v13, v182
	v_mul_f32_e32 v10, v10, v182
	v_mul_f32_e32 v11, v11, v182
	v_mul_f32_e32 v8, v8, v182
	v_mul_f32_e32 v9, v9, v182
	v_mul_f32_e32 v6, v6, v182
	v_mul_f32_e32 v7, v7, v182
	v_mul_f32_e32 v4, v4, v182
	v_mul_f32_e32 v5, v5, v182
	v_mul_f32_e32 v151, v151, v182
.LBB0_1324:
	v_sub_f32_e32 v70, v70, v203
	v_exp_f32_e32 v209, v70
	v_sub_f32_e32 v70, v87, v203
	v_exp_f32_e32 v210, v70
	v_sub_f32_e32 v70, v71, v203
	v_exp_f32_e32 v211, v70
	v_sub_f32_e32 v70, v88, v203
	v_sub_f32_e32 v84, v84, v203
	v_exp_f32_e32 v71, v70
	v_sub_f32_e32 v70, v72, v203
	v_sub_f32_e32 v72, v73, v203
	v_exp_f32_e32 v204, v84
	v_exp_f32_e32 v84, v72
	v_sub_f32_e32 v72, v90, v203
	v_sub_f32_e32 v69, v69, v203
	v_exp_f32_e32 v73, v72
	v_sub_f32_e32 v72, v74, v203
	v_sub_f32_e32 v74, v75, v203
	v_exp_f32_e32 v206, v69
	v_sub_f32_e32 v69, v86, v203
	v_exp_f32_e32 v86, v74
	v_sub_f32_e32 v74, v92, v203
	v_exp_f32_e32 v183, v74
	v_sub_f32_e32 v74, v76, v203
	v_exp_f32_e32 v185, v74
	v_sub_f32_e32 v74, v93, v203
	v_exp_f32_e32 v182, v74
	v_sub_f32_e32 v74, v77, v203
	v_exp_f32_e32 v184, v74
	v_sub_f32_e32 v74, v94, v203
	v_exp_f32_e32 v93, v74
	v_sub_f32_e32 v74, v78, v203
	v_exp_f32_e32 v187, v74
	v_sub_f32_e32 v74, v95, v203
	v_exp_f32_e32 v92, v74
	v_sub_f32_e32 v74, v79, v203
	v_exp_f32_e32 v186, v74
	v_sub_f32_e32 v74, v96, v203
	v_exp_f32_e32 v79, v74
	v_sub_f32_e32 v74, v80, v203
	v_exp_f32_e32 v95, v74
	v_sub_f32_e32 v74, v97, v203
	v_exp_f32_e32 v78, v74
	v_sub_f32_e32 v74, v81, v203
	v_exp_f32_e32 v94, v74
	v_sub_f32_e32 v74, v98, v203
	v_exp_f32_e32 v81, v74
	v_sub_f32_e32 v74, v82, v203
	v_sub_f32_e32 v68, v68, v203
	v_exp_f32_e32 v97, v74
	v_sub_f32_e32 v74, v99, v203
	v_exp_f32_e32 v205, v68
	v_sub_f32_e32 v68, v85, v203
	v_exp_f32_e32 v85, v70
	v_exp_f32_e32 v87, v72
	v_exp_f32_e32 v80, v74
	v_sub_f32_e32 v74, v83, v203
	v_exp_f32_e32 v96, v74
	v_sub_f32_e32 v70, v89, v203
	v_exp_f32_e32 v70, v70
	v_exp_f32_e32 v68, v68
	v_pk_mov_b32 v[74:75], v[84:85], v[84:85] op_sel:[1,0]
	v_pk_mov_b32 v[76:77], v[86:87], v[86:87] op_sel:[1,0]
	v_exp_f32_e32 v69, v69
	v_add_f32_e32 v190, v78, v94
	v_add_f32_e32 v191, v79, v95
	v_add_f32_e32 v192, v80, v96
	v_add_f32_e32 v193, v81, v97
	v_cvt_pk_bf16_f32 v74, v74, v75
	v_cvt_pk_bf16_f32 v75, v76, v77
	v_pk_mov_b32 v[76:77], v[182:183], v[182:183] op_sel:[1,0]
	v_pk_mov_b32 v[82:83], v[92:93], v[92:93] op_sel:[1,0]
	v_pk_mov_b32 v[78:79], v[78:79], v[78:79] op_sel:[1,0]
	v_pk_mov_b32 v[80:81], v[80:81], v[80:81] op_sel:[1,0]
	v_cvt_pk_bf16_f32 v76, v76, v77
	v_cvt_pk_bf16_f32 v77, v82, v83
	v_cvt_pk_bf16_f32 v78, v78, v79
	v_cvt_pk_bf16_f32 v79, v80, v81
	v_pk_mov_b32 v[80:81], v[184:185], v[184:185] op_sel:[1,0]
	v_pk_mov_b32 v[82:83], v[186:187], v[186:187] op_sel:[1,0]
	v_add_f32_e32 v207, v204, v205
	v_add_f32_e32 v88, v70, v84
	v_add_f32_e32 v89, v71, v85
	v_cvt_pk_bf16_f32 v80, v80, v81
	v_cvt_pk_bf16_f32 v81, v82, v83
	v_pk_mov_b32 v[82:83], v[94:95], v[94:95] op_sel:[1,0]
	v_pk_mov_b32 v[84:85], v[96:97], v[96:97] op_sel:[1,0]
	v_add_f32_e32 v208, v68, v206
	v_sub_f32_e32 v72, v91, v203
	v_cvt_pk_bf16_f32 v82, v82, v83
	v_cvt_pk_bf16_f32 v83, v84, v85
	v_add_f32_e32 v84, 0, v207
	v_exp_f32_e32 v72, v72
	v_add_f32_e32 v212, v69, v209
	v_add_f32_e32 v84, v208, v84
	v_add_f32_e32 v213, v210, v211
	v_add_f32_e32 v84, v212, v84
	v_add_f32_e32 v84, v213, v84
	v_add_f32_e32 v84, v89, v84
	v_add_f32_e32 v90, v72, v86
	v_add_f32_e32 v91, v73, v87
	v_add_f32_e32 v84, v88, v84
	v_add_f32_e32 v84, v91, v84
	v_add_f32_e32 v98, v182, v184
	v_add_f32_e32 v99, v183, v185
	v_add_f32_e32 v84, v90, v84
	v_add_f32_e32 v84, v99, v84
	v_add_f32_e32 v188, v92, v186
	v_add_f32_e32 v189, v93, v187
	v_add_f32_e32 v84, v98, v84
	v_add3_u32 v183, s24, v169, v1
	v_add_f32_e32 v84, v189, v84
	v_add_u32_e32 v96, 0x4000, v183
	v_add_f32_e32 v182, v188, v84
	ds_read2_b64 v[84:87], v96 offset0:128 offset1:130
	ds_read2_b64 v[88:91], v96 offset0:132 offset1:134
	ds_read2_b64 v[92:95], v96 offset0:136 offset1:138
	ds_read2_b64 v[96:99], v96 offset0:140 offset1:142
	v_add_f32_e32 v182, v191, v182
	v_add_f32_e32 v182, v190, v182
	v_pk_mov_b32 v[70:71], v[70:71], v[70:71] op_sel:[1,0]
	v_pk_mov_b32 v[72:73], v[72:73], v[72:73] op_sel:[1,0]
	v_add_f32_e32 v182, v193, v182
	v_cvt_pk_bf16_f32 v68, v204, v68
	v_cvt_pk_bf16_f32 v69, v69, v210
	v_cvt_pk_bf16_f32 v70, v70, v71
	v_cvt_pk_bf16_f32 v71, v72, v73
	v_cvt_pk_bf16_f32 v72, v205, v206
	v_cvt_pk_bf16_f32 v73, v209, v211
	v_add_f32_e32 v182, v192, v182
	s_waitcnt lgkmcnt(0)
	v_mfma_f32_32x32x16_bf16 v[52:67], v[84:87], v[68:71], v[52:67]
	v_mfma_f32_32x32x16_bf16 v[52:67], v[88:91], v[76:79], v[52:67]
	v_mfma_f32_32x32x16_bf16 v[52:67], v[92:95], v[72:75], v[52:67]
	v_mfma_f32_32x32x16_bf16 v[52:67], v[96:99], v[80:83], v[52:67]
	v_add_u32_e32 v96, 0x5000, v183
	ds_read2_b64 v[84:87], v96 offset0:160 offset1:162
	ds_read2_b64 v[88:91], v96 offset0:164 offset1:166
	ds_read2_b64 v[92:95], v96 offset0:168 offset1:170
	ds_read2_b64 v[96:99], v96 offset0:172 offset1:174
	s_waitcnt lgkmcnt(0)
	v_mfma_f32_32x32x16_bf16 v[36:51], v[84:87], v[68:71], v[36:51]
	v_mfma_f32_32x32x16_bf16 v[36:51], v[88:91], v[76:79], v[36:51]
	v_mfma_f32_32x32x16_bf16 v[36:51], v[92:95], v[72:75], v[36:51]
	v_mfma_f32_32x32x16_bf16 v[36:51], v[96:99], v[80:83], v[36:51]
	v_add_u32_e32 v96, 0x6000, v183
	ds_read2_b64 v[84:87], v96 offset0:192 offset1:194
	ds_read2_b64 v[88:91], v96 offset0:196 offset1:198
	ds_read2_b64 v[92:95], v96 offset0:200 offset1:202
	ds_read2_b64 v[96:99], v96 offset0:204 offset1:206
	s_waitcnt lgkmcnt(0)
	v_mfma_f32_32x32x16_bf16 v[20:35], v[84:87], v[68:71], v[20:35]
	v_mfma_f32_32x32x16_bf16 v[20:35], v[88:91], v[76:79], v[20:35]
	v_mfma_f32_32x32x16_bf16 v[20:35], v[92:95], v[72:75], v[20:35]
	v_mfma_f32_32x32x16_bf16 v[20:35], v[96:99], v[80:83], v[20:35]
	v_add_u32_e32 v96, 0x7000, v183
	ds_read2_b64 v[84:87], v96 offset0:224 offset1:226
	ds_read2_b64 v[88:91], v96 offset0:228 offset1:230
	ds_read2_b64 v[92:95], v96 offset0:232 offset1:234
	ds_read2_b64 v[96:99], v96 offset0:236 offset1:238
	s_waitcnt lgkmcnt(0)
	v_mfma_f32_32x32x16_bf16 v[4:19], v[84:87], v[68:71], v[4:19]
	v_mfma_f32_32x32x16_bf16 v[4:19], v[88:91], v[76:79], v[4:19]
	v_mfma_f32_32x32x16_bf16 v[4:19], v[92:95], v[72:75], v[4:19]
	v_mfma_f32_32x32x16_bf16 v[4:19], v[96:99], v[80:83], v[4:19]
	v_add_f32_e32 v151, v182, v151
	s_andn2_b64 vcc, exec, s[12:13]
	s_cbranch_vccz .LBB0_1221
	s_branch .LBB0_1222
